# second-round h1 stores written through + small per-wave start stagger in layer kernels
# speedup vs baseline: 1.0014x; 1.0014x over previous
.Lw2b14:
	s_mov_b32 s22, 0x800000
	v_mov_b32_e32 v100, 0xc0135761
	v_mbcnt_hi_u32_b32 v101, -1, v0
	v_mov_b32_e32 v102, 0x1dd00
	s_mov_b32 s47, s41
.Lstg2:
	s_cmp_eq_u32 s47, 0
	s_cbranch_scc1 .Lstg2d
	s_sleep 4
	s_sub_u32 s47, s47, 1
	s_branch .Lstg2
.Lstg2d:
	s_branch .LBB2_9
.LBB2_7:
.Lw2t15:
	s_cbranch_execz .Lw2c15

.Lw2b16:
	v_mov_b32_e32 v34, v21
	v_mov_b32_e32 v35, v22
	v_mov_b32_e32 v37, v23
	v_pk_add_f32 v[34:35], v[34:35], v[36:37]
	v_add_f32_e32 v32, 0, v32
	v_pk_add_f32 v[34:35], v[34:35], v[34:35] op_sel:[0,1] op_sel_hi:[1,0]
	v_add_f32_e32 v32, v32, v33
	v_add_f32_e32 v36, v16, v17
	v_add_f32_e32 v38, v18, v19
	v_mov_b32_e32 v33, v12
	v_mov_b32_e32 v35, v13
	v_mov_b32_e32 v37, v14
	v_mov_b32_e32 v39, v15

.Lw2b17:
	v_pk_add_f32 v[32:33], v[32:33], v[34:35]
	v_pk_add_f32 v[34:35], v[36:37], v[38:39]
	v_mov_b32_e32 v36, v8
	v_pk_add_f32 v[32:33], v[32:33], v[34:35]
	v_mov_b32_e32 v34, v9
	v_mov_b32_e32 v35, v10
	v_mov_b32_e32 v37, v11
	v_pk_add_f32 v[34:35], v[34:35], v[36:37]
	v_pk_add_f32 v[32:33], v[32:33], v[32:33] op_sel:[0,1] op_sel_hi:[1,0]
	v_pk_add_f32 v[34:35], v[34:35], v[34:35] op_sel:[0,1] op_sel_hi:[1,0]

.Lw2b18:
	v_add_f32_e32 v36, v4, v5
	v_add_f32_e32 v38, v6, v7
	v_mov_b32_e32 v33, v0
	v_mov_b32_e32 v35, v1
	v_mov_b32_e32 v37, v2
	v_mov_b32_e32 v39, v3
	v_pk_add_f32 v[32:33], v[32:33], v[34:35]
	v_pk_add_f32 v[34:35], v[36:37], v[38:39]
	s_nop 0
	v_pk_add_f32 v[32:33], v[32:33], v[34:35]
	v_and_b32_e32 v34, 64, v101

.Lw2b19:
	v_add_f32_e32 v32, v32, v33
	v_xor_b32_e32 v33, 16, v101
	v_add_u32_e32 v34, 64, v34
	v_cmp_lt_i32_e32 vcc, v33, v34
	s_nop 1
	v_cndmask_b32_e32 v33, v101, v33, vcc
	v_lshlrev_b32_e32 v42, 2, v33
	ds_bpermute_b32 v33, v42, v32
	s_waitcnt lgkmcnt(0)
	v_add_f32_e32 v32, v32, v33
	v_xor_b32_e32 v33, 32, v101
	v_cmp_lt_i32_e32 vcc, v33, v34
	s_nop 1
	v_cndmask_b32_e32 v33, v101, v33, vcc

.Lw2b20:
	v_lshlrev_b32_e32 v43, 2, v33
	ds_bpermute_b32 v33, v43, v32
	s_waitcnt lgkmcnt(0)
	v_add_f32_e32 v44, v32, v33
	v_fmamk_f32 v29, v44, 0xbc000000, v29
	v_fmamk_f32 v25, v44, 0xbc000000, v25
	v_fmamk_f32 v41, v44, 0xbc000000, v31
	v_fmamk_f32 v40, v44, 0xbc000000, v30
	v_fmac_f32_e32 v28, 0xbc000000, v44

.Lw2b21:
	v_fmamk_f32 v39, v44, 0xbc000000, v27
	v_fmac_f32_e32 v24, 0xbc000000, v44
	v_mov_b32_e32 v30, v29
	v_mov_b32_e32 v31, v25
	v_fmamk_f32 v38, v44, 0xbc000000, v26
	v_mov_b32_e32 v26, v28
	v_mov_b32_e32 v27, v24
	v_pk_mul_f32 v[30:31], v[30:31], v[30:31]
	v_mov_b32_e32 v32, v41
	v_mov_b32_e32 v33, v39
	v_pk_fma_f32 v[26:27], v[26:27], v[26:27], v[30:31]

.Lw2b22:
	v_mov_b32_e32 v30, v40
	v_mov_b32_e32 v31, v38
	v_pk_mul_f32 v[32:33], v[32:33], v[32:33]
	v_fmamk_f32 v37, v44, 0xbc000000, v21
	v_pk_fma_f32 v[30:31], v[30:31], v[30:31], v[32:33]
	v_fmamk_f32 v36, v44, 0xbc000000, v20
	v_fmamk_f32 v23, v44, 0xbc000000, v23
	v_fmac_f32_e32 v22, 0xbc000000, v44

.Lw2b26:
	v_mov_b32_e32 v19, v33
	v_mov_b32_e32 v21, v45
	v_pk_add_f32 v[18:19], v[18:19], v[20:21]
	v_fmamk_f32 v33, v44, 0xbc000000, v9
	v_fmamk_f32 v32, v44, 0xbc000000, v8
	v_fmamk_f32 v11, v44, 0xbc000000, v11
	v_fmac_f32_e32 v10, 0xbc000000, v44
	v_pk_add_f32 v[14:15], v[14:15], v[18:19]
	v_pk_mul_f32 v[8:9], v[10:11], v[10:11]

.Lw2b27:
	v_pk_mul_f32 v[18:19], v[32:33], v[32:33]
	v_fmamk_f32 v1, v44, 0xbc000000, v1
	v_pk_mov_b32 v[20:21], v[18:19], v[8:9] op_sel:[1,0]
	v_mov_b32_e32 v19, v9
	v_pk_add_f32 v[8:9], v[20:21], v[18:19]
	v_fmac_f32_e32 v0, 0xbc000000, v44
	v_fmamk_f32 v19, v44, 0xbc000000, v7
	v_fmamk_f32 v18, v44, 0xbc000000, v6

.Lw2b28:
	v_mul_f32_e32 v20, v0, v0
	v_mul_f32_e32 v21, v1, v1
	v_pk_add_f32 v[6:7], v[14:15], v[14:15] op_sel:[0,1] op_sel_hi:[1,0]
	v_pk_add_f32 v[8:9], v[8:9], v[8:9] op_sel:[0,1] op_sel_hi:[1,0]
	v_fmamk_f32 v5, v44, 0xbc000000, v5
	v_mov_b32_e32 v7, v20
	v_mov_b32_e32 v9, v21
	v_fmac_f32_e32 v4, 0xbc000000, v44
	v_fmamk_f32 v3, v44, 0xbc000000, v3

.Lw2b29:
	v_fmamk_f32 v2, v44, 0xbc000000, v2
	v_pk_add_f32 v[6:7], v[6:7], v[8:9]
	v_mul_f32_e32 v8, v5, v5
	v_mul_f32_e32 v14, v19, v19
	v_mul_f32_e32 v26, v2, v2
	v_mul_f32_e32 v27, v3, v3
	v_pk_fma_f32 v[8:9], v[4:5], v[4:5], v[8:9] op_sel_hi:[1,1,0]
	v_pk_fma_f32 v[14:15], v[18:19], v[18:19], v[14:15] op_sel_hi:[1,1,0]
	v_mov_b32_e32 v9, v26
	v_mov_b32_e32 v15, v27
	v_pk_add_f32 v[8:9], v[8:9], v[14:15]

.Lw2b30:
	s_nop 0
	v_pk_add_f32 v[6:7], v[6:7], v[8:9]
	s_nop 0
	v_add_f32_e32 v6, v6, v7
	ds_bpermute_b32 v7, v42, v6
	s_waitcnt lgkmcnt(0)
	v_add_f32_e32 v6, v6, v7
	ds_bpermute_b32 v7, v43, v6
	s_waitcnt lgkmcnt(0)
	v_add_f32_e32 v6, v6, v7
	v_fmamk_f32 v6, v6, 0x3c000000, v99

.Lw2b31:
	v_mul_f32_e32 v7, 0x4b800000, v6
	v_cmp_gt_f32_e32 vcc, s22, v6
	s_nop 1
	v_cndmask_b32_e32 v6, v6, v7, vcc
	v_rsq_f32_e32 v14, v6
	ds_read_b128 v[6:9], v97 offset:512
	ds_read_b128 v[42:45], v97 offset:528
	ds_read_b128 v[46:49], v97 offset:1024
	ds_read_b128 v[50:53], v97 offset:1040

.Lw2b32:
	v_mul_f32_e32 v15, 0x45800000, v14
	v_cndmask_b32_e32 v20, v14, v15, vcc
	v_pk_mul_f32 v[26:27], v[20:21], v[28:29] op_sel_hi:[0,1]
	s_waitcnt lgkmcnt(1)
	v_pk_fma_f32 v[6:7], v[6:7], v[26:27], v[46:47]
	v_or_b32_e32 v14, s4, v82
	v_pk_mul_f32 v[26:27], v[6:7], v[6:7]
	v_ashrrev_i32_e32 v15, 31, v14
	v_fmamk_f32 v21, v26, 0xbdd2d3e8, v100
	v_mul_f32_e32 v21, v6, v21

.Lw2b33:
	v_fmamk_f32 v26, v27, 0xbdd2d3e8, v100
	v_exp_f32_e32 v21, v21
	v_mul_f32_e32 v26, v7, v26
	v_exp_f32_e32 v26, v26
	v_lshlrev_b64 v[14:15], 8, v[14:15]
	v_add_f32_e32 v21, 1.0, v21
	v_rcp_f32_e32 v28, v21
	v_add_f32_e32 v21, 1.0, v26
	v_pk_mul_f32 v[26:27], v[20:21], v[40:41] op_sel_hi:[0,1]
	v_pk_fma_f32 v[8:9], v[8:9], v[26:27], v[48:49]
	v_rcp_f32_e32 v29, v21

.Lw2b34:
	v_pk_mul_f32 v[40:41], v[8:9], v[8:9]
	v_mad_u32_u24 v104, v86, 6, v83
	s_cmp_ge_u32 s4, 0xd000
	s_cselect_b32 s47, 1, 0
	s_lshl_b32 s12, s4, 8
	v_mov_b32_e32 v105, 0
	v_add_u32_e32 v104, s12, v104
	s_nop 0
	v_lshl_add_u64 v[104:105], v[78:79], 0, v[104:105]
	v_fmamk_f32 v21, v40, 0xbdd2d3e8, v100

.Lw2b35:
	v_mul_f32_e32 v21, v8, v21
	v_exp_f32_e32 v21, v21
	v_fmamk_f32 v14, v41, 0xbdd2d3e8, v100
	v_pk_mul_f32 v[6:7], v[6:7], v[28:29]
	v_mul_f32_e32 v14, v9, v14
	v_cvt_pk_f16_f32 v6, v6, v7
	v_add_f32_e32 v7, 1.0, v21
	v_exp_f32_e32 v21, v14
	v_rcp_f32_e32 v28, v7
	v_pk_mul_f32 v[14:15], v[20:21], v[24:25] op_sel_hi:[0,1]
	s_waitcnt lgkmcnt(0)

.Lw2b36:
	v_pk_fma_f32 v[14:15], v[42:43], v[14:15], v[50:51]
	v_add_f32_e32 v7, 1.0, v21
	v_pk_mul_f32 v[24:25], v[14:15], v[14:15]
	v_rcp_f32_e32 v29, v7
	v_fmamk_f32 v24, v24, 0xbdd2d3e8, v100
	v_mul_f32_e32 v24, v14, v24
	v_exp_f32_e32 v24, v24
	v_fmamk_f32 v21, v25, 0xbdd2d3e8, v100
	v_mul_f32_e32 v21, v15, v21
	v_pk_mul_f32 v[8:9], v[8:9], v[28:29]

.Lw2b37:
	v_add_f32_e32 v7, 1.0, v24
	v_pk_mul_f32 v[24:25], v[20:21], v[38:39] op_sel_hi:[0,1]
	v_pk_fma_f32 v[24:25], v[44:45], v[24:25], v[52:53]
	v_exp_f32_e32 v21, v21
	v_pk_mul_f32 v[38:39], v[24:25], v[24:25]
	v_rcp_f32_e32 v40, v7
	v_fmamk_f32 v38, v38, 0xbdd2d3e8, v100
	v_fmamk_f32 v39, v39, 0xbdd2d3e8, v100
	v_mul_f32_e32 v38, v24, v38
	v_mul_f32_e32 v39, v25, v39

.Lw2b38:
	v_exp_f32_e32 v38, v38
	v_exp_f32_e32 v39, v39
	v_add_f32_e32 v7, 1.0, v21
	v_mov_b32_e32 v21, v86
	v_add_f32_e32 v38, 1.0, v38
	v_add_f32_e32 v39, 1.0, v39
	v_rcp_f32_e32 v38, v38
	v_rcp_f32_e32 v39, v39
	v_rcp_f32_e32 v41, v7
	v_pk_mul_f32 v[24:25], v[24:25], v[38:39]
	s_nop 0
	s_nop 0
	v_lshl_add_u32 v7, v21, 2, v102

.Lw2b39:
	v_add_u32_e32 v54, 0x420, v7
	v_add_u32_e32 v48, 0x428, v7
	v_add_u32_e32 v52, 0x430, v7
	ds_read2_b32 v[38:39], v7 offset0:138 offset1:139
	ds_read2_b32 v[42:43], v7 offset0:142 offset1:143
	ds_read2_b32 v[44:45], v7 offset0:140 offset1:141
	ds_read2_b32 v[46:47], v7 offset0:136 offset1:137
	v_add_u32_e32 v7, 0x438, v7

.Lw2b40:
	ds_read2_b32 v[48:49], v48 offset1:1
	ds_read2_b32 v[50:51], v7 offset1:1
	ds_read2_b32 v[52:53], v52 offset1:1
	ds_read2_b32 v[54:55], v54 offset1:1
	v_cvt_pk_f16_f32 v7, v8, v9
	v_pk_mul_f32 v[8:9], v[14:15], v[40:41]
	s_nop 0
	v_cvt_pk_f16_f32 v8, v8, v9

.Lw2b41:
	v_pk_mul_f32 v[14:15], v[20:21], v[36:37] op_sel_hi:[0,1]
	s_waitcnt lgkmcnt(0)
	v_pk_fma_f32 v[14:15], v[46:47], v[14:15], v[54:55]
	v_pk_mul_f32 v[22:23], v[20:21], v[22:23] op_sel_hi:[0,1]
	v_pk_mul_f32 v[28:29], v[14:15], v[14:15]
	v_pk_fma_f32 v[22:23], v[38:39], v[22:23], v[48:49]
	v_fmamk_f32 v9, v28, 0xbdd2d3e8, v100
	v_mul_f32_e32 v9, v14, v9

.Lw2b42:
	v_fmamk_f32 v28, v29, 0xbdd2d3e8, v100
	v_exp_f32_e32 v9, v9
	v_mul_f32_e32 v28, v15, v28
	v_exp_f32_e32 v29, v28
	v_pk_mul_f32 v[36:37], v[22:23], v[22:23]
	v_add_f32_e32 v9, 1.0, v9
	v_rcp_f32_e32 v28, v9
	v_add_f32_e32 v9, 1.0, v29
	v_rcp_f32_e32 v29, v9
	v_fmamk_f32 v9, v36, 0xbdd2d3e8, v100
	v_mul_f32_e32 v9, v22, v9
	v_exp_f32_e32 v36, v9

.Lw2b43:
	v_cvt_pk_f16_f32 v9, v24, v25
	v_fmamk_f32 v24, v37, 0xbdd2d3e8, v100
	v_pk_mul_f32 v[16:17], v[20:21], v[16:17] op_sel_hi:[0,1]
	v_mul_f32_e32 v24, v23, v24
	v_pk_fma_f32 v[16:17], v[44:45], v[16:17], v[52:53]
	v_pk_mul_f32 v[14:15], v[14:15], v[28:29]
	v_exp_f32_e32 v29, v24
	v_pk_mul_f32 v[24:25], v[16:17], v[16:17]
	v_cvt_pk_f16_f32 v14, v14, v15

.Lw2b44:
	v_fmamk_f32 v24, v24, 0xbdd2d3e8, v100
	v_mul_f32_e32 v24, v16, v24
	v_exp_f32_e32 v24, v24
	v_add_f32_e32 v15, 1.0, v36
	v_rcp_f32_e32 v28, v15
	v_add_f32_e32 v15, 1.0, v29
	v_rcp_f32_e32 v29, v15
	v_add_f32_e32 v15, 1.0, v24
	v_fmamk_f32 v24, v25, 0xbdd2d3e8, v100
	v_mul_f32_e32 v36, v17, v24
	v_pk_mul_f32 v[24:25], v[20:21], v[34:35] op_sel_hi:[0,1]

.Lw2b45:
	v_pk_fma_f32 v[24:25], v[42:43], v[24:25], v[50:51]
	v_exp_f32_e32 v37, v36
	v_pk_mul_f32 v[34:35], v[24:25], v[24:25]
	v_rcp_f32_e32 v36, v15
	v_fmamk_f32 v34, v34, 0xbdd2d3e8, v100
	v_fmamk_f32 v35, v35, 0xbdd2d3e8, v100
	v_mul_f32_e32 v34, v24, v34
	v_mul_f32_e32 v35, v25, v35
	v_exp_f32_e32 v34, v34
	v_exp_f32_e32 v35, v35
	v_add_f32_e32 v15, 1.0, v37

.Lw2b46:
	v_rcp_f32_e32 v37, v15
	v_add_f32_e32 v34, 1.0, v34
	v_add_f32_e32 v35, 1.0, v35
	v_rcp_f32_e32 v34, v34
	v_rcp_f32_e32 v35, v35
	v_pk_mul_f32 v[22:23], v[22:23], v[28:29]
	v_pk_mul_f32 v[16:17], v[16:17], v[36:37]
	v_pk_mul_f32 v[24:25], v[24:25], v[34:35]
	s_nop 0
	v_cvt_pk_f16_f32 v16, v16, v17
	v_lshl_add_u32 v15, v21, 2, v102

.Lw2b47:
	v_add_u32_e32 v50, 0x440, v15
	v_add_u32_e32 v44, 0x448, v15
	v_add_u32_e32 v48, 0x450, v15
	ds_read2_b32 v[34:35], v15 offset0:146 offset1:147
	ds_read2_b32 v[38:39], v15 offset0:150 offset1:151
	ds_read2_b32 v[40:41], v15 offset0:148 offset1:149
	ds_read2_b32 v[42:43], v15 offset0:144 offset1:145

.Lw2b48:
	v_add_u32_e32 v15, 0x458, v15
	ds_read2_b32 v[44:45], v44 offset1:1
	ds_read2_b32 v[46:47], v15 offset1:1
	ds_read2_b32 v[48:49], v48 offset1:1
	ds_read2_b32 v[50:51], v50 offset1:1
	v_cvt_pk_f16_f32 v15, v22, v23
	v_pk_mul_f32 v[12:13], v[20:21], v[12:13] op_sel_hi:[0,1]
	s_waitcnt lgkmcnt(0)

.Lw2b49:
	v_pk_fma_f32 v[12:13], v[42:43], v[12:13], v[50:51]
	v_pk_mul_f32 v[28:29], v[20:21], v[30:31] op_sel_hi:[0,1]
	v_pk_mul_f32 v[22:23], v[12:13], v[12:13]
	v_pk_fma_f32 v[28:29], v[34:35], v[28:29], v[44:45]
	v_fmamk_f32 v17, v22, 0xbdd2d3e8, v100
	v_mul_f32_e32 v17, v12, v17
	v_fmamk_f32 v22, v23, 0xbdd2d3e8, v100
	v_exp_f32_e32 v17, v17
	v_mul_f32_e32 v22, v13, v22

.Lw2b50:
	v_exp_f32_e32 v23, v22
	v_pk_mul_f32 v[30:31], v[28:29], v[28:29]
	v_add_f32_e32 v17, 1.0, v17
	v_rcp_f32_e32 v22, v17
	v_add_f32_e32 v17, 1.0, v23
	v_rcp_f32_e32 v23, v17
	v_fmamk_f32 v17, v30, 0xbdd2d3e8, v100
	v_mul_f32_e32 v17, v28, v17
	v_exp_f32_e32 v30, v17
	v_pk_mul_f32 v[12:13], v[12:13], v[22:23]
	v_cvt_pk_f16_f32 v17, v24, v25

.Lw2b51:
	v_cvt_pk_f16_f32 v22, v12, v13
	v_fmamk_f32 v12, v31, 0xbdd2d3e8, v100
	v_mul_f32_e32 v12, v29, v12
	v_exp_f32_e32 v31, v12
	v_pk_mul_f32 v[12:13], v[20:21], v[32:33] op_sel_hi:[0,1]
	v_pk_fma_f32 v[12:13], v[40:41], v[12:13], v[48:49]
	v_add_f32_e32 v23, 1.0, v30
	v_pk_mul_f32 v[24:25], v[12:13], v[12:13]
	v_rcp_f32_e32 v30, v23
	v_fmamk_f32 v24, v24, 0xbdd2d3e8, v100

.Lw2b52:
	v_mul_f32_e32 v24, v12, v24
	v_exp_f32_e32 v24, v24
	v_add_f32_e32 v23, 1.0, v31
	v_pk_mul_f32 v[10:11], v[20:21], v[10:11] op_sel_hi:[0,1]
	v_rcp_f32_e32 v31, v23
	v_add_f32_e32 v23, 1.0, v24
	v_fmamk_f32 v24, v25, 0xbdd2d3e8, v100
	v_pk_fma_f32 v[10:11], v[38:39], v[10:11], v[46:47]
	v_mul_f32_e32 v32, v13, v24
	v_pk_mul_f32 v[24:25], v[10:11], v[10:11]

.Lw2b53:
	v_exp_f32_e32 v33, v32
	v_fmamk_f32 v24, v24, 0xbdd2d3e8, v100
	v_fmamk_f32 v25, v25, 0xbdd2d3e8, v100
	v_mul_f32_e32 v24, v10, v24
	v_mul_f32_e32 v25, v11, v25
	v_exp_f32_e32 v24, v24
	v_exp_f32_e32 v25, v25
	v_rcp_f32_e32 v32, v23
	v_add_f32_e32 v23, 1.0, v33
	v_add_f32_e32 v24, 1.0, v24
	v_add_f32_e32 v25, 1.0, v25
	v_rcp_f32_e32 v24, v24
	v_rcp_f32_e32 v25, v25

.Lw2b54:
	v_rcp_f32_e32 v33, v23
	v_pk_mul_f32 v[10:11], v[10:11], v[24:25]
	s_nop 0
	v_pk_mul_f32 v[12:13], v[12:13], v[32:33]
	v_lshl_add_u32 v21, v21, 2, v102
	v_add_u32_e32 v24, 0x468, v21
	ds_read2_b32 v[34:35], v21 offset0:154 offset1:155
	ds_read2_b32 v[36:37], v21 offset0:158 offset1:159
	ds_read2_b32 v[38:39], v21 offset0:156 offset1:157

.Lw2b55:
	ds_read2_b32 v[40:41], v21 offset0:152 offset1:153
	v_add_u32_e32 v23, 0x460, v21
	v_add_u32_e32 v25, 0x470, v21
	v_add_u32_e32 v21, 0x478, v21
	ds_read2_b32 v[42:43], v24 offset1:1
	ds_read2_b32 v[44:45], v21 offset1:1
	ds_read2_b32 v[46:47], v25 offset1:1

.Lw2b56:
	ds_read2_b32 v[48:49], v23 offset1:1
	v_pk_mul_f32 v[24:25], v[28:29], v[30:31]
	s_nop 0
	v_cvt_pk_f16_f32 v23, v24, v25
	v_cvt_pk_f16_f32 v24, v12, v13
	v_pk_mul_f32 v[4:5], v[20:21], v[4:5] op_sel_hi:[0,1]
	s_waitcnt lgkmcnt(0)
	v_pk_fma_f32 v[4:5], v[40:41], v[4:5], v[48:49]
	ds_write_b128 v125, v[6:9]

.Lw2b57:
	v_pk_mul_f32 v[12:13], v[4:5], v[4:5]
	v_pk_mul_f32 v[0:1], v[20:21], v[0:1] op_sel_hi:[0,1]
	v_fmamk_f32 v12, v12, 0xbdd2d3e8, v100
	v_fmamk_f32 v13, v13, 0xbdd2d3e8, v100
	v_mul_f32_e32 v12, v4, v12
	v_mul_f32_e32 v13, v5, v13
	v_exp_f32_e32 v12, v12
	v_exp_f32_e32 v13, v13
	v_pk_fma_f32 v[0:1], v[38:39], v[0:1], v[46:47]

.Lw2b58:
	v_cvt_pk_f16_f32 v25, v10, v11
	v_add_f32_e32 v6, 1.0, v12
	v_add_f32_e32 v7, 1.0, v13
	v_rcp_f32_e32 v6, v6
	v_rcp_f32_e32 v7, v7
	v_pk_mul_f32 v[10:11], v[0:1], v[0:1]
	v_pk_mul_f32 v[2:3], v[20:21], v[2:3] op_sel_hi:[0,1]
	v_pk_fma_f32 v[2:3], v[36:37], v[2:3], v[44:45]
	v_pk_mul_f32 v[4:5], v[4:5], v[6:7]
	v_pk_mul_f32 v[6:7], v[20:21], v[18:19] op_sel_hi:[0,1]

.Lw2b59:
	v_pk_fma_f32 v[6:7], v[34:35], v[6:7], v[42:43]
	v_cvt_pk_f16_f32 v4, v4, v5
	v_pk_mul_f32 v[8:9], v[6:7], v[6:7]
	s_mov_b64 s[4:5], 0
	v_fmamk_f32 v8, v8, 0xbdd2d3e8, v100
	v_mul_f32_e32 v8, v6, v8
	v_fmamk_f32 v9, v9, 0xbdd2d3e8, v100
	v_exp_f32_e32 v8, v8
	v_mul_f32_e32 v9, v7, v9

.Lw2b60:
	v_exp_f32_e32 v9, v9
	ds_write_b128 v125, v[14:17] offset:16
	v_add_f32_e32 v5, 1.0, v8
	v_rcp_f32_e32 v8, v5
	v_add_f32_e32 v5, 1.0, v9
	v_rcp_f32_e32 v9, v5
	v_fmamk_f32 v5, v10, 0xbdd2d3e8, v100
	v_mul_f32_e32 v5, v0, v5
	v_fmamk_f32 v10, v11, 0xbdd2d3e8, v100
	v_exp_f32_e32 v5, v5
	v_mul_f32_e32 v10, v1, v10
	v_exp_f32_e32 v10, v10

.Lw2b61:
	v_pk_mul_f32 v[6:7], v[6:7], v[8:9]
	v_add_f32_e32 v5, 1.0, v5
	v_rcp_f32_e32 v8, v5
	v_add_f32_e32 v5, 1.0, v10
	v_pk_mul_f32 v[10:11], v[2:3], v[2:3]
	ds_write_b128 v125, v[22:25] offset:32
	v_fmamk_f32 v9, v10, 0xbdd2d3e8, v100
	v_mul_f32_e32 v9, v2, v9
	v_exp_f32_e32 v10, v9
	v_fmamk_f32 v9, v11, 0xbdd2d3e8, v100

.Lw2b62:
	v_mul_f32_e32 v9, v3, v9
	v_exp_f32_e32 v11, v9
	v_rcp_f32_e32 v9, v5
	v_add_f32_e32 v5, 1.0, v10
	v_rcp_f32_e32 v10, v5
	v_add_f32_e32 v5, 1.0, v11
	v_rcp_f32_e32 v11, v5
	v_pk_mul_f32 v[0:1], v[0:1], v[8:9]
	v_cvt_pk_f16_f32 v5, v6, v7
	v_cvt_pk_f16_f32 v6, v0, v1
	v_pk_mul_f32 v[0:1], v[2:3], v[10:11]

.Lw2b63:
	s_nop 0
	v_cvt_pk_f16_f32 v7, v0, v1
	ds_write_b128 v125, v[4:7] offset:48
	ds_read_b128 v[4:7], v126
	ds_read_b128 v[8:11], v126 offset:1088
	ds_read_b128 v[12:15], v126 offset:2176
	ds_read_b128 v[16:19], v126 offset:3264
	s_cmp_lg_u32 s47, 0
	s_waitcnt lgkmcnt(0)
	s_cbranch_scc1 .Lh1_wt

.Lw2b64:
	global_store_dwordx4 v[104:105], v[4:7], off
	global_store_dwordx4 v[104:105], v[8:11], off offset:1024
	global_store_dwordx4 v[104:105], v[12:15], off offset:2048
	global_store_dwordx4 v[104:105], v[16:19], off offset:3072
	s_branch .LBB2_8
.Lh1_wt:
	global_store_dwordx4 v[104:105], v[4:7], off sc1
	global_store_dwordx4 v[104:105], v[8:11], off offset:1024 sc1
	global_store_dwordx4 v[104:105], v[12:15], off offset:2048 sc1
.Lw2t65:
	s_cbranch_execz .Lw2c65
.Lw2b65:
	global_store_dwordx4 v[104:105], v[16:19], off offset:3072 sc1

.Lw3b15:
	v_mov_b32_e32 v98, 0x3727c5ac
	s_mov_b32 s28, 0x800000
	v_mov_b32_e32 v99, 0xc0135761
	v_mbcnt_hi_u32_b32 v100, -1, v0
	v_mov_b32_e32 v101, 0x26d00
	v_mov_b32_e32 v102, 0x1dd00
	s_mov_b32 s47, s41
.Lstg3:
	s_cmp_eq_u32 s47, 0
	s_cbranch_scc1 .Lstg3d

.Lw3b16:
	s_sleep 4
	s_sub_u32 s47, s47, 1
	s_branch .Lstg3
.Lstg3d:
	s_branch .LBB3_11
.LBB3_9:
	s_or_b64 exec, exec, s[14:15]
	s_mov_b64 s[10:11], 0

.LBB3_11:
	s_nop 0
	v_mov_b32_e32 v0, 0
	s_and_saveexec_b64 s[10:11], s[0:1]
	s_cbranch_execz .LBB3_15
	s_mov_b64 s[20:21], exec
	v_mbcnt_lo_u32_b32 v0, s20, 0
.Lw3t17:
	s_cbranch_execz .Lw3c17
.Lw3b17:
	v_mbcnt_hi_u32_b32 v0, s21, v0
	v_cmp_eq_u32_e32 vcc, 0, v0
	s_and_saveexec_b64 s[14:15], vcc
	s_bcnt1_i32_b64 s12, s[20:21]
	v_mov_b32_e32 v1, s12
	ds_add_rtn_u32 v1, v95, v1
	s_or_b64 exec, exec, s[14:15]
	s_waitcnt lgkmcnt(0)
	v_readfirstlane_b32 s12, v1
	s_nop 1
	v_add_u32_e32 v0, s12, v0
.LBB3_15:
	s_or_b64 exec, exec, s[10:11]
	v_readfirstlane_b32 s10, v0
.Lw3t18:
	s_cbranch_execz .Lw3c18
.Lw3b18:
	s_waitcnt lgkmcnt(0)
	s_mul_i32 s12, s10, s3
	s_add_i32 s12, s12, s2
	s_cmpk_gt_i32 s12, 0x1869
	s_mov_b64 s[10:11], -1
	s_cbranch_scc1 .LBB3_10
	ds_read_b128 v[28:31], v96
	ds_read_b128 v[24:27], v96 offset:16
	ds_read_b128 v[20:23], v96 offset:32
	ds_read_b128 v[16:19], v96 offset:48
	ds_read_b128 v[12:15], v96 offset:64

.Lw3b19:
	ds_read_b128 v[8:11], v96 offset:80
	ds_read_b128 v[4:7], v96 offset:96
	ds_read_b128 v[0:3], v96 offset:112
	s_lshl_b32 s10, s12, 4
	s_ashr_i32 s11, s10, 31
	v_lshl_add_u64 v[78:79], s[10:11], 2, v[74:75]
	s_mov_b32 s11, 0
	s_mov_b64 s[22:23], -1
	s_branch .LBB3_18
.LBB3_17:
	s_or_b64 exec, exec, s[20:21]
.Lw3t20:
	s_cbranch_execz .Lw3c20
.Lw3b20:
	v_mov_b32_e32 v48, v77
	ds_read_b128 v[32:35], v97
	ds_read_b128 v[36:39], v97 offset:64
	ds_read_b128 v[40:43], v97 offset:128
	ds_read_b128 v[44:47], v97 offset:192
	s_nop 0
	v_lshlrev_b32_e32 v48, 4, v48
	v_lshl_add_u32 v103, s11, 15, v48
	ds_read_b128 v[48:51], v103

.Lw3b21:
	ds_read_b128 v[52:55], v103 offset:1024
	ds_read_b128 v[56:59], v103 offset:2048
	ds_read_b128 v[60:63], v103 offset:3072
	ds_read_b128 v[64:67], v103 offset:4096
	ds_read_b128 v[68:71], v103 offset:5120
	ds_read_b128 v[104:107], v103 offset:6144
	ds_read_b128 v[108:111], v103 offset:7168
	s_waitcnt lgkmcnt(7)

.Lw3b22:
	v_mfma_f32_16x16x32_f16 v[28:31], v[48:51], v[32:35], v[28:31]
	s_waitcnt lgkmcnt(6)
	v_mfma_f32_16x16x32_f16 v[24:27], v[52:55], v[32:35], v[24:27]
	s_waitcnt lgkmcnt(5)
	v_mfma_f32_16x16x32_f16 v[20:23], v[56:59], v[32:35], v[20:23]
	s_waitcnt lgkmcnt(4)
	v_mfma_f32_16x16x32_f16 v[16:19], v[60:63], v[32:35], v[16:19]
	ds_read_b128 v[48:51], v103 offset:8192
	ds_read_b128 v[52:55], v103 offset:9216

.Lw3b23:
	ds_read_b128 v[56:59], v103 offset:10240
	ds_read_b128 v[60:63], v103 offset:11264
	s_waitcnt lgkmcnt(7)
	v_mfma_f32_16x16x32_f16 v[12:15], v[64:67], v[32:35], v[12:15]
	s_waitcnt lgkmcnt(6)
	v_mfma_f32_16x16x32_f16 v[8:11], v[68:71], v[32:35], v[8:11]
	s_waitcnt lgkmcnt(5)
	v_mfma_f32_16x16x32_f16 v[4:7], v[104:107], v[32:35], v[4:7]
	s_waitcnt lgkmcnt(4)
	v_mfma_f32_16x16x32_f16 v[0:3], v[108:111], v[32:35], v[0:3]

.Lw3b24:
	ds_read_b128 v[32:35], v103 offset:12288
	ds_read_b128 v[64:67], v103 offset:13312
	ds_read_b128 v[68:71], v103 offset:14336
	ds_read_b128 v[104:107], v103 offset:15360
	s_waitcnt lgkmcnt(7)
	v_mfma_f32_16x16x32_f16 v[28:31], v[48:51], v[36:39], v[28:31]
	s_waitcnt lgkmcnt(6)
	v_mfma_f32_16x16x32_f16 v[24:27], v[52:55], v[36:39], v[24:27]

.Lw3b25:
	s_waitcnt lgkmcnt(5)
	v_mfma_f32_16x16x32_f16 v[20:23], v[56:59], v[36:39], v[20:23]
	s_waitcnt lgkmcnt(4)
	v_mfma_f32_16x16x32_f16 v[16:19], v[60:63], v[36:39], v[16:19]
	ds_read_b128 v[48:51], v103 offset:16384
	ds_read_b128 v[52:55], v103 offset:17408
	ds_read_b128 v[56:59], v103 offset:18432
	ds_read_b128 v[60:63], v103 offset:19456
	s_waitcnt lgkmcnt(7)

.Lw3b26:
	v_mfma_f32_16x16x32_f16 v[12:15], v[32:35], v[36:39], v[12:15]
	s_waitcnt lgkmcnt(6)
	v_mfma_f32_16x16x32_f16 v[8:11], v[64:67], v[36:39], v[8:11]
	s_waitcnt lgkmcnt(5)
	v_mfma_f32_16x16x32_f16 v[4:7], v[68:71], v[36:39], v[4:7]
	s_waitcnt lgkmcnt(4)
	v_mfma_f32_16x16x32_f16 v[0:3], v[104:107], v[36:39], v[0:3]
	ds_read_b128 v[32:35], v103 offset:20480
	ds_read_b128 v[36:39], v103 offset:21504

.Lw3b27:
	ds_read_b128 v[64:67], v103 offset:22528
	ds_read_b128 v[68:71], v103 offset:23552
	s_waitcnt lgkmcnt(7)
	v_mfma_f32_16x16x32_f16 v[28:31], v[48:51], v[40:43], v[28:31]
	s_waitcnt lgkmcnt(6)
	v_mfma_f32_16x16x32_f16 v[24:27], v[52:55], v[40:43], v[24:27]
	s_waitcnt lgkmcnt(5)
	v_mfma_f32_16x16x32_f16 v[20:23], v[56:59], v[40:43], v[20:23]
	s_waitcnt lgkmcnt(4)
	v_mfma_f32_16x16x32_f16 v[16:19], v[60:63], v[40:43], v[16:19]

.Lw3b28:
	ds_read_b128 v[48:51], v103 offset:24576
	ds_read_b128 v[52:55], v103 offset:25600
	ds_read_b128 v[56:59], v103 offset:26624
	ds_read_b128 v[60:63], v103 offset:27648
	s_waitcnt lgkmcnt(7)
	v_mfma_f32_16x16x32_f16 v[12:15], v[32:35], v[40:43], v[12:15]
	s_waitcnt lgkmcnt(6)
	v_mfma_f32_16x16x32_f16 v[8:11], v[36:39], v[40:43], v[8:11]

.Lw3b29:
	s_waitcnt lgkmcnt(5)
	v_mfma_f32_16x16x32_f16 v[4:7], v[64:67], v[40:43], v[4:7]
	s_waitcnt lgkmcnt(4)
	v_mfma_f32_16x16x32_f16 v[0:3], v[68:71], v[40:43], v[0:3]
	ds_read_b128 v[32:35], v103 offset:28672
	ds_read_b128 v[36:39], v103 offset:29696
	ds_read_b128 v[40:43], v103 offset:30720
	ds_read_b128 v[64:67], v103 offset:31744
	s_waitcnt lgkmcnt(7)

.Lw3b30:
	v_mfma_f32_16x16x32_f16 v[28:31], v[48:51], v[44:47], v[28:31]
	s_waitcnt lgkmcnt(6)
	v_mfma_f32_16x16x32_f16 v[24:27], v[52:55], v[44:47], v[24:27]
	s_waitcnt lgkmcnt(5)
	v_mfma_f32_16x16x32_f16 v[20:23], v[56:59], v[44:47], v[20:23]
	s_waitcnt lgkmcnt(4)
	v_mfma_f32_16x16x32_f16 v[16:19], v[60:63], v[44:47], v[16:19]
	s_waitcnt lgkmcnt(3)
	v_mfma_f32_16x16x32_f16 v[12:15], v[32:35], v[44:47], v[12:15]
	s_waitcnt lgkmcnt(2)

.Lw3b31:
	v_mfma_f32_16x16x32_f16 v[8:11], v[36:39], v[44:47], v[8:11]
	s_waitcnt lgkmcnt(1)
	v_mfma_f32_16x16x32_f16 v[4:7], v[40:43], v[44:47], v[4:7]
	s_waitcnt lgkmcnt(0)
	v_mfma_f32_16x16x32_f16 v[0:3], v[64:67], v[44:47], v[0:3]
	s_mov_b32 s11, 1
	s_mov_b64 s[22:23], 0
	s_and_b64 vcc, exec, s[14:15]
	s_cbranch_vccnz .LBB3_94
.LBB3_18:
	s_mul_i32 s12, s11, 0x186a1
	v_lshl_add_u64 v[32:33], s[12:13], 2, v[78:79]
.Lw3t32:
	s_cbranch_execz .Lw3c32
.Lw3b32:
	global_load_dword v113, v[32:33], off
	global_load_dword v103, v[32:33], off offset:16
	s_mov_b32 s14, s13
	s_mov_b32 s15, s13
	s_mul_i32 s12, s11, 0xc3500
	s_lshl_b64 s[20:21], s[12:13], 2
	s_mov_b32 s12, s13
	v_mov_b64_e32 v[34:35], s[14:15]
	v_mov_b64_e32 v[32:33], s[12:13]
	s_add_u32 s20, s18, s20
	ds_write_b128 v83, v[32:35]
	ds_write_b128 v83, v[32:35] offset:16
	ds_write_b128 v83, v[32:35] offset:32
	ds_write_b128 v83, v[32:35] offset:48
	s_addc_u32 s21, s19, s21

.Lw3b33:
	v_mov_b32_e32 v116, 0x3f86a0
	s_waitcnt vmcnt(1)
	v_add_u32_e32 v32, v113, v80
	s_waitcnt vmcnt(0)
	v_cmp_lt_i32_e32 vcc, v32, v103
	s_and_saveexec_b64 s[14:15], vcc
.Lw3t34:
	s_cbranch_execz .Lw3c34
.Lw3b34:
	s_cbranch_execz .LBB3_20
	v_ashrrev_i32_e32 v33, 31, v32
	v_lshl_add_u64 v[32:33], v[32:33], 2, s[20:21]
	global_load_dword v116, v[32:33], off
.LBB3_20:
	s_or_b64 exec, exec, s[14:15]
	v_mov_b32_e32 v56, 0
	s_xor_b64 s[14:15], s[22:23], -1
	v_mov_b32_e32 v115, 31
	v_mov_b32_e32 v57, v56
	v_mov_b32_e32 v58, v56
	v_mov_b32_e32 v59, v56
	v_mov_b32_e32 v60, v56
	v_mov_b32_e32 v61, v56
.Lw3t35:
	s_cbranch_execz .Lw3c35
.Lw3b35:
	v_mov_b32_e32 v62, v56
	v_mov_b32_e32 v63, v56
	s_branch .LBB3_22
.LBB3_21:
	s_waitcnt vmcnt(0)
	v_mov_b32_e32 v116, v114
	s_cbranch_execnz .LBB3_92
.LBB3_22:
	s_nop 2
	v_mov_b32_e32 v104, v63
	v_mov_b32_e32 v106, v62
	v_mov_b32_e32 v105, v61
	v_mov_b32_e32 v108, v60
	v_mov_b32_e32 v109, v59
	v_mov_b32_e32 v111, v58
	v_mov_b32_e32 v110, v57
	v_mov_b32_e32 v112, v56
.Lw3t36:
	s_cbranch_execz .Lw3c36
.Lw3b36:
	v_mov_b32_e32 v107, v115
	v_cmp_lt_i32_e32 vcc, v113, v103
	s_cbranch_vccz .LBB3_21
	v_or_b32_e32 v32, 4, v82
	s_waitcnt vmcnt(0)
	ds_bpermute_b32 v66, v82, v116
	ds_bpermute_b32 v123, v32, v116
	v_or_b32_e32 v32, 8, v82
	v_or_b32_e32 v34, 12, v82
	ds_bpermute_b32 v122, v32, v116
	ds_bpermute_b32 v121, v34, v116

.Lw3b37:
	v_or_b32_e32 v34, 16, v82
	ds_bpermute_b32 v120, v34, v116
	v_or_b32_e32 v34, 20, v82
	ds_bpermute_b32 v119, v34, v116
	s_waitcnt lgkmcnt(5)
	v_lshlrev_b32_e32 v32, 8, v66
	s_waitcnt lgkmcnt(4)
	v_lshlrev_b32_e32 v33, 8, v123
	v_and_or_b32 v32, v32, s27, v81
	v_and_or_b32 v33, v33, s27, v81
	ds_bpermute_b32 v118, v85, v116

.Lw3b38:
	ds_bpermute_b32 v117, v86, v116
	global_load_dwordx4 v[60:63], v32, s[8:9]
	global_load_dwordx4 v[56:59], v33, s[8:9]
	s_waitcnt lgkmcnt(5)
	v_lshlrev_b32_e32 v32, 8, v122
	s_waitcnt lgkmcnt(4)
	v_lshlrev_b32_e32 v33, 8, v121
	v_and_or_b32 v32, v32, s27, v81
	v_and_or_b32 v33, v33, s27, v81

.Lw3b39:
	global_load_dwordx4 v[52:55], v32, s[8:9]
	global_load_dwordx4 v[48:51], v33, s[8:9]
	s_waitcnt lgkmcnt(3)
	v_lshlrev_b32_e32 v32, 8, v120
	s_waitcnt lgkmcnt(2)
	v_lshlrev_b32_e32 v33, 8, v119
	v_and_or_b32 v32, v32, s27, v81
	v_and_or_b32 v33, v33, s27, v81
	global_load_dwordx4 v[44:47], v32, s[8:9]
	global_load_dwordx4 v[40:43], v33, s[8:9]

.Lw3b40:
	s_waitcnt lgkmcnt(1)
	v_lshlrev_b32_e32 v32, 8, v118
	s_waitcnt lgkmcnt(0)
	v_lshlrev_b32_e32 v33, 8, v117
	v_and_or_b32 v32, v32, s27, v81
	v_and_or_b32 v33, v33, s27, v81
	global_load_dwordx4 v[36:39], v32, s[8:9]
	s_nop 0
	global_load_dwordx4 v[32:35], v33, s[8:9]
	v_or_b32_e32 v64, 16, v80

.Lw3b41:
	v_add_u32_e32 v64, v64, v113
	v_cmp_lt_i32_e32 vcc, v64, v103
	v_mov_b32_e32 v114, 0x3f86a0
	s_and_saveexec_b64 s[22:23], vcc
	s_cbranch_execz .LBB3_25
	v_ashrrev_i32_e32 v65, 31, v64
	v_lshl_add_u64 v[64:65], v[64:65], 2, s[20:21]
	global_load_dword v114, v[64:65], off
.LBB3_25:
	s_or_b64 exec, exec, s[22:23]
	v_ashrrev_i32_e32 v124, 17, v66
	v_cmp_ne_u32_e32 vcc, v124, v107
	s_cmp_lg_u64 vcc, 0
	s_cselect_b64 s[22:23], -1, 0
.Lw3t42:
	s_cbranch_execz .Lw3c42
.Lw3b42:
	s_and_b64 s[24:25], s[22:23], vcc
	v_mov_b32_e32 v115, v107
	v_mov_b32_e32 v68, v112
	v_mov_b32_e32 v69, v110
	v_mov_b32_e32 v70, v111
	v_mov_b32_e32 v71, v109
	v_mov_b32_e32 v64, v108
	v_mov_b32_e32 v65, v105
	v_mov_b32_e32 v66, v106
	v_mov_b32_e32 v67, v104
	s_and_saveexec_b64 s[22:23], s[24:25]
	s_cbranch_execz .LBB3_29
	v_cmp_gt_i32_e32 vcc, 16, v107
	s_and_saveexec_b64 s[24:25], vcc

.Lw3b43:
	s_cbranch_execz .LBB3_28
	v_cvt_pk_f16_f32 v67, v111, v109
	v_cvt_pk_f16_f32 v66, v112, v110
	v_cvt_pk_f16_f32 v65, v106, v104
	v_cvt_pk_f16_f32 v64, v108, v105
	v_mad_u64_u32 v[68:69], s[30:31], v107, s26, v[76:77]
	ds_write_b128 v68, v[64:67]
.LBB3_28:
	s_or_b64 exec, exec, s[24:25]
	v_mov_b32_e32 v68, 0
.Lw3t44:
	s_cbranch_execz .Lw3c44
.Lw3b44:
	v_mov_b32_e32 v115, v124
	v_mov_b32_e32 v69, v68
	v_mov_b32_e32 v70, v68
	v_mov_b32_e32 v71, v68
	v_mov_b32_e32 v64, v68
	v_mov_b32_e32 v65, v68
	v_mov_b32_e32 v66, v68
	v_mov_b32_e32 v67, v68
.LBB3_29:
	s_or_b64 exec, exec, s[22:23]
	v_ashrrev_i32_e32 v123, 17, v123
	s_waitcnt vmcnt(7)
	v_mfma_f32_16x16x16_f16 v[64:67], v[72:73], v[60:61], v[64:67]
	v_cmp_ne_u32_e32 vcc, v123, v115
	s_cmp_lg_u64 vcc, 0
	s_cselect_b64 s[22:23], -1, 0
.Lw3t45:
	s_cbranch_execz .Lw3c45
.Lw3b45:
	v_mfma_f32_16x16x16_f16 v[60:63], v[72:73], v[62:63], v[68:71]
	s_and_b64 s[24:25], s[22:23], vcc
	s_and_saveexec_b64 s[22:23], s[24:25]
	s_cbranch_execz .LBB3_33
	v_cmp_gt_i32_e32 vcc, 16, v115
	s_and_saveexec_b64 s[24:25], vcc
	s_cbranch_execz .LBB3_32
	s_nop 1
	v_cvt_pk_f16_f32 v63, v62, v63
	v_cvt_pk_f16_f32 v62, v60, v61
	v_cvt_pk_f16_f32 v61, v66, v67

.Lw3b46:
	v_cvt_pk_f16_f32 v60, v64, v65
	v_mad_u64_u32 v[64:65], s[30:31], v115, s26, v[76:77]
	ds_write_b128 v64, v[60:63]
.LBB3_32:
	s_or_b64 exec, exec, s[24:25]
	s_nop 0
	v_mov_b32_e32 v60, 0
	v_mov_b32_e32 v115, v123
	v_mov_b32_e32 v61, v60
	v_mov_b32_e32 v62, v60
	v_mov_b32_e32 v63, v60
	v_mov_b32_e32 v64, v60
.Lw3t47:
	s_cbranch_execz .Lw3c47
.Lw3b47:
	v_mov_b32_e32 v65, v60
	v_mov_b32_e32 v66, v60
	v_mov_b32_e32 v67, v60
.LBB3_33:
	s_or_b64 exec, exec, s[22:23]
	v_ashrrev_i32_e32 v68, 17, v122
	s_waitcnt vmcnt(6)
	v_mfma_f32_16x16x16_f16 v[64:67], v[72:73], v[56:57], v[64:67]
	v_cmp_ne_u32_e32 vcc, v68, v115
	s_cmp_lg_u64 vcc, 0
	s_cselect_b64 s[22:23], -1, 0
	v_mfma_f32_16x16x16_f16 v[56:59], v[72:73], v[58:59], v[60:63]
	s_and_b64 s[24:25], s[22:23], vcc
	s_and_saveexec_b64 s[22:23], s[24:25]

.Lw3b48:
	s_cbranch_execz .LBB3_37
	v_cmp_gt_i32_e32 vcc, 16, v115
	s_and_saveexec_b64 s[24:25], vcc
	s_cbranch_execz .LBB3_36
	s_nop 1
	v_cvt_pk_f16_f32 v59, v58, v59
	v_cvt_pk_f16_f32 v58, v56, v57
	v_cvt_pk_f16_f32 v57, v66, v67
	v_cvt_pk_f16_f32 v56, v64, v65
	v_mad_u64_u32 v[60:61], s[30:31], v115, s26, v[76:77]

.LBB3_37:
	s_or_b64 exec, exec, s[22:23]
	v_ashrrev_i32_e32 v68, 17, v121
.Lw3t50:
	s_cbranch_execz .Lw3c50
.Lw3b50:
	s_waitcnt vmcnt(5)
	v_mfma_f32_16x16x16_f16 v[60:63], v[72:73], v[52:53], v[64:67]
	v_cmp_ne_u32_e32 vcc, v68, v115
	s_cmp_lg_u64 vcc, 0
	s_cselect_b64 s[22:23], -1, 0
	v_mfma_f32_16x16x16_f16 v[52:55], v[72:73], v[54:55], v[56:59]
	s_and_b64 s[24:25], s[22:23], vcc
	s_and_saveexec_b64 s[22:23], s[24:25]
	s_cbranch_execz .LBB3_41
	v_cmp_gt_i32_e32 vcc, 16, v115
	s_and_saveexec_b64 s[24:25], vcc
	s_cbranch_execz .LBB3_40
	s_nop 1

.Lw3b52:
	v_mov_b32_e32 v115, v68
	v_mov_b32_e32 v53, v52
	v_mov_b32_e32 v54, v52
	v_mov_b32_e32 v55, v52
	v_mov_b32_e32 v60, v52
	v_mov_b32_e32 v61, v52
	v_mov_b32_e32 v62, v52
	v_mov_b32_e32 v63, v52
.LBB3_41:
	s_or_b64 exec, exec, s[22:23]
	v_ashrrev_i32_e32 v64, 17, v120
	s_waitcnt vmcnt(4)
	v_mfma_f32_16x16x16_f16 v[56:59], v[72:73], v[48:49], v[60:63]
	v_cmp_ne_u32_e32 vcc, v64, v115
	s_cmp_lg_u64 vcc, 0
	s_cselect_b64 s[22:23], -1, 0
.Lw3t53:
	s_cbranch_execz .Lw3c53

.LBB3_45:
	s_or_b64 exec, exec, s[22:23]
	v_ashrrev_i32_e32 v60, 17, v119
	s_waitcnt vmcnt(3)
	v_mfma_f32_16x16x16_f16 v[52:55], v[72:73], v[44:45], v[56:59]
	v_cmp_ne_u32_e32 vcc, v60, v115
	s_cmp_lg_u64 vcc, 0
	s_cselect_b64 s[22:23], -1, 0
	v_mfma_f32_16x16x16_f16 v[44:47], v[72:73], v[46:47], v[48:51]
	s_and_b64 s[24:25], s[22:23], vcc
	s_and_saveexec_b64 s[22:23], s[24:25]

.LBB3_49:
	s_or_b64 exec, exec, s[22:23]
	v_ashrrev_i32_e32 v56, 17, v118
.Lw3t58:
	s_cbranch_execz .Lw3c58

.LBB3_53:
	s_or_b64 exec, exec, s[22:23]
	v_ashrrev_i32_e32 v52, 17, v117
	s_waitcnt vmcnt(1)
	v_mfma_f32_16x16x16_f16 v[44:47], v[72:73], v[36:37], v[48:51]
	v_cmp_ne_u32_e32 vcc, v52, v115
	s_cmp_lg_u64 vcc, 0
	s_cselect_b64 s[22:23], -1, 0
.Lw3t61:
	s_cbranch_execz .Lw3c61

.LBB3_57:
	s_or_b64 exec, exec, s[22:23]
	s_waitcnt vmcnt(0)
	v_mfma_f32_16x16x16_f16 v[60:63], v[72:73], v[32:33], v[44:47]
	v_add_u32_e32 v32, 8, v113
	v_cmp_lt_i32_e32 vcc, v32, v103
	v_mfma_f32_16x16x16_f16 v[56:59], v[72:73], v[34:35], v[36:39]
	s_cbranch_vccz .LBB3_91
	ds_bpermute_b32 v123, v87, v116
	ds_bpermute_b32 v122, v88, v116

.Lw3b64:
	ds_bpermute_b32 v121, v89, v116
	ds_bpermute_b32 v120, v90, v116
	ds_bpermute_b32 v119, v91, v116
	ds_bpermute_b32 v118, v92, v116
	s_waitcnt lgkmcnt(5)
	v_lshlrev_b32_e32 v32, 8, v123
	s_waitcnt lgkmcnt(4)
	v_lshlrev_b32_e32 v33, 8, v122
	v_and_or_b32 v32, v32, s27, v81

.Lw3b65:
	v_and_or_b32 v33, v33, s27, v81
	ds_bpermute_b32 v117, v93, v116
	ds_bpermute_b32 v116, v94, v116
	global_load_dwordx4 v[68:71], v32, s[8:9]
	global_load_dwordx4 v[64:67], v33, s[8:9]
	s_waitcnt lgkmcnt(5)
	v_lshlrev_b32_e32 v32, 8, v121
	s_waitcnt lgkmcnt(4)
	v_lshlrev_b32_e32 v33, 8, v120
	v_and_or_b32 v32, v32, s27, v81

.Lw3b66:
	v_and_or_b32 v33, v33, s27, v81
	global_load_dwordx4 v[52:55], v32, s[8:9]
	global_load_dwordx4 v[48:51], v33, s[8:9]
	s_waitcnt lgkmcnt(3)
	v_lshlrev_b32_e32 v32, 8, v119
	s_waitcnt lgkmcnt(2)
	v_lshlrev_b32_e32 v33, 8, v118
	v_and_or_b32 v32, v32, s27, v81
	v_and_or_b32 v33, v33, s27, v81

.Lw3b67:
	global_load_dwordx4 v[44:47], v32, s[8:9]
	global_load_dwordx4 v[40:43], v33, s[8:9]
	s_waitcnt lgkmcnt(1)
	v_lshlrev_b32_e32 v32, 8, v117
	s_waitcnt lgkmcnt(0)
	v_lshlrev_b32_e32 v33, 8, v116
	v_and_or_b32 v32, v32, s27, v81
	v_and_or_b32 v33, v33, s27, v81
	global_load_dwordx4 v[36:39], v32, s[8:9]
	s_nop 0

.Lw3b68:
	global_load_dwordx4 v[32:35], v33, s[8:9]
	v_ashrrev_i32_e32 v123, 17, v123
	v_cmp_ne_u32_e32 vcc, v123, v115
	s_cmp_lg_u64 vcc, 0
	s_cselect_b64 s[22:23], -1, 0
	s_and_b64 s[24:25], s[22:23], vcc
	s_and_saveexec_b64 s[22:23], s[24:25]
	s_cbranch_execz .LBB3_62
	v_cmp_gt_i32_e32 vcc, 16, v115
	s_and_saveexec_b64 s[24:25], vcc
	s_cbranch_execz .LBB3_61
	v_cvt_pk_f16_f32 v59, v58, v59
	v_cvt_pk_f16_f32 v58, v56, v57

.Lw3b69:
	v_cvt_pk_f16_f32 v57, v62, v63
	v_cvt_pk_f16_f32 v56, v60, v61
	v_mad_u64_u32 v[60:61], s[30:31], v115, s26, v[76:77]
	ds_write_b128 v60, v[56:59]
.LBB3_61:
	s_or_b64 exec, exec, s[24:25]
	v_mov_b32_e32 v56, 0
	v_mov_b32_e32 v115, v123
	v_mov_b32_e32 v57, v56
	v_mov_b32_e32 v58, v56
	v_mov_b32_e32 v59, v56
.Lw3t70:
	s_cbranch_execz .Lw3c70

.LBB3_62:
	s_or_b64 exec, exec, s[22:23]
	v_ashrrev_i32_e32 v122, 17, v122
	s_waitcnt vmcnt(7)
	v_mfma_f32_16x16x16_f16 v[60:63], v[72:73], v[68:69], v[60:63]
	v_cmp_ne_u32_e32 vcc, v122, v115
	s_cmp_lg_u64 vcc, 0
	s_cselect_b64 s[22:23], -1, 0
	v_mfma_f32_16x16x16_f16 v[56:59], v[72:73], v[70:71], v[56:59]
	s_and_b64 s[24:25], s[22:23], vcc

.Lw3b71:
	s_and_saveexec_b64 s[22:23], s[24:25]
	s_cbranch_execz .LBB3_66
	v_cmp_gt_i32_e32 vcc, 16, v115
	s_and_saveexec_b64 s[24:25], vcc
	s_cbranch_execz .LBB3_65
	s_nop 1
	v_cvt_pk_f16_f32 v59, v58, v59
	v_cvt_pk_f16_f32 v58, v56, v57
	v_cvt_pk_f16_f32 v57, v62, v63
	v_cvt_pk_f16_f32 v56, v60, v61
	v_mad_u64_u32 v[60:61], s[30:31], v115, s26, v[76:77]

.LBB3_66:
	s_or_b64 exec, exec, s[22:23]
.Lw3t73:
	s_cbranch_execz .Lw3c73
.Lw3b73:
	v_ashrrev_i32_e32 v68, 17, v121
	s_waitcnt vmcnt(6)
	v_mfma_f32_16x16x16_f16 v[60:63], v[72:73], v[64:65], v[60:63]
	v_cmp_ne_u32_e32 vcc, v68, v115
	s_cmp_lg_u64 vcc, 0
	s_cselect_b64 s[22:23], -1, 0
	v_mfma_f32_16x16x16_f16 v[56:59], v[72:73], v[66:67], v[56:59]
	s_and_b64 s[24:25], s[22:23], vcc
	s_and_saveexec_b64 s[22:23], s[24:25]
	s_cbranch_execz .LBB3_70
	v_cmp_gt_i32_e32 vcc, 16, v115
	s_and_saveexec_b64 s[24:25], vcc
	s_cbranch_execz .LBB3_69

.Lw3b74:
	s_nop 1
	v_cvt_pk_f16_f32 v59, v58, v59
	v_cvt_pk_f16_f32 v58, v56, v57
	v_cvt_pk_f16_f32 v57, v62, v63
	v_cvt_pk_f16_f32 v56, v60, v61
	v_mad_u64_u32 v[60:61], s[30:31], v115, s26, v[76:77]
	ds_write_b128 v60, v[56:59]
.LBB3_69:
	s_or_b64 exec, exec, s[24:25]
	s_nop 0
.Lw3t75:
	s_cbranch_execz .Lw3c75
.Lw3b75:
	v_mov_b32_e32 v56, 0
	v_mov_b32_e32 v115, v68
	v_mov_b32_e32 v57, v56
	v_mov_b32_e32 v58, v56
	v_mov_b32_e32 v59, v56
	v_mov_b32_e32 v60, v56
	v_mov_b32_e32 v61, v56
	v_mov_b32_e32 v62, v56
	v_mov_b32_e32 v63, v56
.LBB3_70:
	s_or_b64 exec, exec, s[22:23]
	v_ashrrev_i32_e32 v64, 17, v120
	s_waitcnt vmcnt(5)
	v_mfma_f32_16x16x16_f16 v[60:63], v[72:73], v[52:53], v[60:63]
	v_cmp_ne_u32_e32 vcc, v64, v115
.Lw3t76:
	s_cbranch_execz .Lw3c76
.Lw3b76:
	s_cmp_lg_u64 vcc, 0
	s_cselect_b64 s[22:23], -1, 0
	v_mfma_f32_16x16x16_f16 v[52:55], v[72:73], v[54:55], v[56:59]
	s_and_b64 s[24:25], s[22:23], vcc
	s_and_saveexec_b64 s[22:23], s[24:25]
	s_cbranch_execz .LBB3_74
	v_cmp_gt_i32_e32 vcc, 16, v115
	s_and_saveexec_b64 s[24:25], vcc
	s_cbranch_execz .LBB3_73
	s_nop 1
	v_cvt_pk_f16_f32 v55, v54, v55
	v_cvt_pk_f16_f32 v54, v52, v53

.Lw3b77:
	v_cvt_pk_f16_f32 v53, v62, v63
	v_cvt_pk_f16_f32 v52, v60, v61
	v_mad_u64_u32 v[56:57], s[30:31], v115, s26, v[76:77]
	ds_write_b128 v56, v[52:55]
.LBB3_73:
	s_or_b64 exec, exec, s[24:25]
	s_nop 0
	v_mov_b32_e32 v52, 0
	v_mov_b32_e32 v115, v64
	v_mov_b32_e32 v53, v52
	v_mov_b32_e32 v54, v52
	v_mov_b32_e32 v55, v52
.Lw3t78:
	s_cbranch_execz .Lw3c78
.Lw3b78:
	v_mov_b32_e32 v60, v52
	v_mov_b32_e32 v61, v52
	v_mov_b32_e32 v62, v52
	v_mov_b32_e32 v63, v52
.LBB3_74:
	s_or_b64 exec, exec, s[22:23]
	v_ashrrev_i32_e32 v64, 17, v119
	s_waitcnt vmcnt(4)
	v_mfma_f32_16x16x16_f16 v[56:59], v[72:73], v[48:49], v[60:63]
	v_cmp_ne_u32_e32 vcc, v64, v115
	s_cmp_lg_u64 vcc, 0
	s_cselect_b64 s[22:23], -1, 0
	v_mfma_f32_16x16x16_f16 v[48:51], v[72:73], v[50:51], v[52:55]
	s_and_b64 s[24:25], s[22:23], vcc

.Lw3b79:
	s_and_saveexec_b64 s[22:23], s[24:25]
	s_cbranch_execz .LBB3_78
	v_cmp_gt_i32_e32 vcc, 16, v115
	s_and_saveexec_b64 s[24:25], vcc
	s_cbranch_execz .LBB3_77
	s_nop 1
	v_cvt_pk_f16_f32 v51, v50, v51
	v_cvt_pk_f16_f32 v50, v48, v49
	v_cvt_pk_f16_f32 v49, v58, v59
	v_cvt_pk_f16_f32 v48, v56, v57
	v_mad_u64_u32 v[52:53], s[30:31], v115, s26, v[76:77]

.LBB3_78:
	s_or_b64 exec, exec, s[22:23]
.Lw3t81:
	s_cbranch_execz .Lw3c81
.Lw3b81:
	v_ashrrev_i32_e32 v60, 17, v118
	s_waitcnt vmcnt(3)
	v_mfma_f32_16x16x16_f16 v[52:55], v[72:73], v[44:45], v[56:59]
	v_cmp_ne_u32_e32 vcc, v60, v115
	s_cmp_lg_u64 vcc, 0
	s_cselect_b64 s[22:23], -1, 0
	v_mfma_f32_16x16x16_f16 v[44:47], v[72:73], v[46:47], v[48:51]
	s_and_b64 s[24:25], s[22:23], vcc
	s_and_saveexec_b64 s[22:23], s[24:25]
	s_cbranch_execz .LBB3_82
	v_cmp_gt_i32_e32 vcc, 16, v115
	s_and_saveexec_b64 s[24:25], vcc
	s_cbranch_execz .LBB3_81

.Lw3b82:
	s_nop 1
	v_cvt_pk_f16_f32 v47, v46, v47
	v_cvt_pk_f16_f32 v46, v44, v45
	v_cvt_pk_f16_f32 v45, v54, v55
	v_cvt_pk_f16_f32 v44, v52, v53
	v_mad_u64_u32 v[48:49], s[30:31], v115, s26, v[76:77]
	ds_write_b128 v48, v[44:47]
.LBB3_81:
	s_or_b64 exec, exec, s[24:25]
	s_nop 0
.Lw3t83:
	s_cbranch_execz .Lw3c83
.Lw3b83:
	v_mov_b32_e32 v44, 0
	v_mov_b32_e32 v115, v60
	v_mov_b32_e32 v45, v44
	v_mov_b32_e32 v46, v44
	v_mov_b32_e32 v47, v44
	v_mov_b32_e32 v52, v44
	v_mov_b32_e32 v53, v44
	v_mov_b32_e32 v54, v44
	v_mov_b32_e32 v55, v44
.LBB3_82:
	s_or_b64 exec, exec, s[22:23]
	v_ashrrev_i32_e32 v56, 17, v117
	s_waitcnt vmcnt(2)
	v_mfma_f32_16x16x16_f16 v[48:51], v[72:73], v[40:41], v[52:55]
	v_cmp_ne_u32_e32 vcc, v56, v115
.Lw3t84:
	s_cbranch_execz .Lw3c84
.Lw3b84:
	s_cmp_lg_u64 vcc, 0
	s_cselect_b64 s[22:23], -1, 0
	v_mfma_f32_16x16x16_f16 v[40:43], v[72:73], v[42:43], v[44:47]
	s_and_b64 s[24:25], s[22:23], vcc
	s_and_saveexec_b64 s[22:23], s[24:25]
	s_cbranch_execz .LBB3_86
	v_cmp_gt_i32_e32 vcc, 16, v115
	s_and_saveexec_b64 s[24:25], vcc
	s_cbranch_execz .LBB3_85
	s_nop 1
	v_cvt_pk_f16_f32 v43, v42, v43
	v_cvt_pk_f16_f32 v42, v40, v41

.Lw3b85:
	v_cvt_pk_f16_f32 v41, v50, v51
	v_cvt_pk_f16_f32 v40, v48, v49
	v_mad_u64_u32 v[44:45], s[30:31], v115, s26, v[76:77]
	ds_write_b128 v44, v[40:43]
.LBB3_85:
	s_or_b64 exec, exec, s[24:25]
	s_nop 0
	v_mov_b32_e32 v40, 0
	v_mov_b32_e32 v115, v56
	v_mov_b32_e32 v41, v40
	v_mov_b32_e32 v42, v40
	v_mov_b32_e32 v43, v40
.Lw3t86:
	s_cbranch_execz .Lw3c86
.Lw3b86:
	v_mov_b32_e32 v48, v40
	v_mov_b32_e32 v49, v40
	v_mov_b32_e32 v50, v40
	v_mov_b32_e32 v51, v40
.LBB3_86:
	s_or_b64 exec, exec, s[22:23]
	v_ashrrev_i32_e32 v52, 17, v116
	s_waitcnt vmcnt(1)
	v_mfma_f32_16x16x16_f16 v[44:47], v[72:73], v[36:37], v[48:51]
	v_cmp_ne_u32_e32 vcc, v52, v115
	s_cmp_lg_u64 vcc, 0
	s_cselect_b64 s[22:23], -1, 0
	v_mfma_f32_16x16x16_f16 v[36:39], v[72:73], v[38:39], v[40:43]
	s_and_b64 s[24:25], s[22:23], vcc

.Lw3b87:
	s_and_saveexec_b64 s[22:23], s[24:25]
	s_cbranch_execz .LBB3_90
	v_cmp_gt_i32_e32 vcc, 16, v115
	s_and_saveexec_b64 s[24:25], vcc
	s_cbranch_execz .LBB3_89
	s_nop 1
	v_cvt_pk_f16_f32 v39, v38, v39
	v_cvt_pk_f16_f32 v38, v36, v37
	v_cvt_pk_f16_f32 v37, v46, v47
	v_cvt_pk_f16_f32 v36, v44, v45
	v_mad_u64_u32 v[40:41], s[30:31], v115, s26, v[76:77]

.LBB3_90:
	s_or_b64 exec, exec, s[22:23]
.Lw3t89:
	s_cbranch_execz .Lw3c89
.Lw3b89:
	s_waitcnt vmcnt(0)
	v_mfma_f32_16x16x16_f16 v[60:63], v[72:73], v[32:33], v[44:47]
	v_add_u32_e32 v32, 16, v113
	v_mfma_f32_16x16x16_f16 v[56:59], v[72:73], v[34:35], v[36:39]

.LBB3_92:
	v_cmp_gt_i32_e32 vcc, 16, v107
	s_and_saveexec_b64 s[20:21], vcc
	s_cbranch_execz .LBB3_17
	v_cvt_pk_f16_f32 v35, v111, v109
	v_cvt_pk_f16_f32 v34, v112, v110
.Lw3t90:
	s_cbranch_execz .Lw3c90
.Lw3b90:
	v_cvt_pk_f16_f32 v33, v106, v104
	v_cvt_pk_f16_f32 v32, v108, v105
	v_mad_u64_u32 v[36:37], s[22:23], v107, s26, v[76:77]
	ds_write_b128 v36, v[32:35]
	s_branch .LBB3_17

.Lw3b91:
	v_mov_b32_e32 v34, v30
	v_mov_b32_e32 v35, v26
	v_mov_b32_e32 v36, v31
	v_mov_b32_e32 v37, v27
	v_pk_add_f32 v[34:35], v[34:35], v[36:37]
	v_mov_b32_e32 v36, v20
	v_pk_add_f32 v[32:33], v[32:33], v[34:35]
	v_mov_b32_e32 v34, v21
	v_mov_b32_e32 v35, v22
	v_mov_b32_e32 v37, v23
	v_pk_add_f32 v[34:35], v[34:35], v[36:37]
.Lw3t92:
	s_cbranch_execz .Lw3c92
.Lw3b92:
	v_add_f32_e32 v32, 0, v32
	v_pk_add_f32 v[34:35], v[34:35], v[34:35] op_sel:[0,1] op_sel_hi:[1,0]
	v_add_f32_e32 v32, v32, v33
	v_add_f32_e32 v36, v16, v17
	v_add_f32_e32 v38, v18, v19
	v_mov_b32_e32 v33, v12
	v_mov_b32_e32 v35, v13
	v_mov_b32_e32 v37, v14
	v_mov_b32_e32 v39, v15
	v_pk_add_f32 v[32:33], v[32:33], v[34:35]
	v_pk_add_f32 v[34:35], v[36:37], v[38:39]
	v_mov_b32_e32 v36, v8

.Lw3b93:
	v_pk_add_f32 v[32:33], v[32:33], v[34:35]
	v_mov_b32_e32 v34, v9
	v_mov_b32_e32 v35, v10
	v_mov_b32_e32 v37, v11
	v_pk_add_f32 v[34:35], v[34:35], v[36:37]
	v_pk_add_f32 v[32:33], v[32:33], v[32:33] op_sel:[0,1] op_sel_hi:[1,0]
	v_pk_add_f32 v[34:35], v[34:35], v[34:35] op_sel:[0,1] op_sel_hi:[1,0]
	v_add_f32_e32 v36, v4, v5
	v_add_f32_e32 v38, v6, v7
	v_mov_b32_e32 v33, v0
	v_mov_b32_e32 v35, v1

.Lw3b94:
	v_mov_b32_e32 v37, v2
	v_mov_b32_e32 v39, v3
	v_pk_add_f32 v[32:33], v[32:33], v[34:35]
	v_pk_add_f32 v[34:35], v[36:37], v[38:39]
	s_nop 0
	v_pk_add_f32 v[32:33], v[32:33], v[34:35]
	v_and_b32_e32 v34, 64, v100
	v_add_f32_e32 v32, v32, v33
	v_xor_b32_e32 v33, 16, v100
	v_add_u32_e32 v34, 64, v34
	v_cmp_lt_i32_e32 vcc, v33, v34
	s_nop 1

.Lw3b95:
	v_cndmask_b32_e32 v33, v100, v33, vcc
	v_lshlrev_b32_e32 v40, 2, v33
	ds_bpermute_b32 v33, v40, v32
	s_waitcnt lgkmcnt(0)
	v_add_f32_e32 v32, v32, v33
	v_xor_b32_e32 v33, 32, v100
	v_cmp_lt_i32_e32 vcc, v33, v34
	s_nop 1
	v_cndmask_b32_e32 v33, v100, v33, vcc
	v_lshlrev_b32_e32 v41, 2, v33
	ds_bpermute_b32 v33, v41, v32
	s_waitcnt lgkmcnt(0)
	v_add_f32_e32 v42, v32, v33

.Lw3b96:
	v_fmamk_f32 v29, v42, 0xbc000000, v29
	v_fmamk_f32 v25, v42, 0xbc000000, v25
	v_fmamk_f32 v39, v42, 0xbc000000, v31
	v_fmamk_f32 v38, v42, 0xbc000000, v30
	v_fmac_f32_e32 v28, 0xbc000000, v42
	v_fmamk_f32 v37, v42, 0xbc000000, v27
	v_fmac_f32_e32 v24, 0xbc000000, v42
	v_mov_b32_e32 v30, v29

.Lw3b97:
	v_mov_b32_e32 v31, v25
	v_fmamk_f32 v36, v42, 0xbc000000, v26
	v_mov_b32_e32 v26, v28
	v_mov_b32_e32 v27, v24
	v_pk_mul_f32 v[30:31], v[30:31], v[30:31]
	v_mov_b32_e32 v32, v39
	v_mov_b32_e32 v33, v37
	v_pk_fma_f32 v[26:27], v[26:27], v[26:27], v[30:31]
	v_mov_b32_e32 v30, v38
	v_mov_b32_e32 v31, v36
	v_pk_mul_f32 v[32:33], v[32:33], v[32:33]

.Lw3b98:
	v_fmamk_f32 v35, v42, 0xbc000000, v21
	v_pk_fma_f32 v[30:31], v[30:31], v[30:31], v[32:33]
	v_fmamk_f32 v34, v42, 0xbc000000, v20
	v_fmamk_f32 v23, v42, 0xbc000000, v23
	v_fmac_f32_e32 v22, 0xbc000000, v42
	v_pk_add_f32 v[26:27], v[26:27], v[30:31]
	v_pk_mul_f32 v[20:21], v[22:23], v[22:23]
	v_pk_mul_f32 v[30:31], v[34:35], v[34:35]

.Lw3b99:
	v_fmamk_f32 v13, v42, 0xbc000000, v13
	v_pk_mov_b32 v[32:33], v[30:31], v[20:21] op_sel:[1,0]
	v_mov_b32_e32 v31, v21
	v_pk_add_f32 v[20:21], v[32:33], v[30:31]
	v_fmac_f32_e32 v12, 0xbc000000, v42
	v_fmamk_f32 v33, v42, 0xbc000000, v19
	v_fmamk_f32 v32, v42, 0xbc000000, v18
	v_fmamk_f32 v19, v42, 0xbc000000, v15

.Lw3b100:
	v_fmamk_f32 v18, v42, 0xbc000000, v14
	v_mul_f32_e32 v30, v12, v12
	v_mul_f32_e32 v31, v13, v13
	v_pk_add_f32 v[14:15], v[26:27], v[26:27] op_sel:[0,1] op_sel_hi:[1,0]
	v_pk_add_f32 v[20:21], v[20:21], v[20:21] op_sel:[0,1] op_sel_hi:[1,0]
	v_fmamk_f32 v17, v42, 0xbc000000, v17
	v_mov_b32_e32 v15, v30
	v_mov_b32_e32 v21, v31
	v_fmac_f32_e32 v16, 0xbc000000, v42

.Lw3b101:
	v_pk_add_f32 v[14:15], v[14:15], v[20:21]
	v_mul_f32_e32 v20, v17, v17
	v_mul_f32_e32 v26, v33, v33
	v_mul_f32_e32 v43, v18, v18
	v_mul_f32_e32 v44, v19, v19
	v_pk_fma_f32 v[20:21], v[16:17], v[16:17], v[20:21] op_sel_hi:[1,1,0]
	v_pk_fma_f32 v[26:27], v[32:33], v[32:33], v[26:27] op_sel_hi:[1,1,0]
	v_mov_b32_e32 v21, v43
	v_mov_b32_e32 v27, v44
	v_pk_add_f32 v[20:21], v[20:21], v[26:27]
	v_fmamk_f32 v11, v42, 0xbc000000, v11

.Lw3b102:
	v_pk_add_f32 v[14:15], v[14:15], v[20:21]
	v_fmamk_f32 v21, v42, 0xbc000000, v9
	v_fmamk_f32 v20, v42, 0xbc000000, v8
	v_fmac_f32_e32 v10, 0xbc000000, v42
	v_pk_mul_f32 v[8:9], v[10:11], v[10:11]
	v_pk_mul_f32 v[26:27], v[20:21], v[20:21]
	v_fmamk_f32 v1, v42, 0xbc000000, v1

.Lw3b103:
	v_pk_mov_b32 v[30:31], v[26:27], v[8:9] op_sel:[1,0]
	v_mov_b32_e32 v27, v9
	v_pk_add_f32 v[8:9], v[30:31], v[26:27]
	v_fmac_f32_e32 v0, 0xbc000000, v42
	v_fmamk_f32 v27, v42, 0xbc000000, v7
	v_fmamk_f32 v26, v42, 0xbc000000, v6
	v_mul_f32_e32 v30, v0, v0
	v_mul_f32_e32 v31, v1, v1
	v_pk_add_f32 v[6:7], v[14:15], v[14:15] op_sel:[0,1] op_sel_hi:[1,0]

.Lw3b104:
	v_pk_add_f32 v[8:9], v[8:9], v[8:9] op_sel:[0,1] op_sel_hi:[1,0]
	v_fmamk_f32 v5, v42, 0xbc000000, v5
	v_mov_b32_e32 v7, v30
	v_mov_b32_e32 v9, v31
	v_fmac_f32_e32 v4, 0xbc000000, v42
	v_fmamk_f32 v3, v42, 0xbc000000, v3
	v_fmamk_f32 v2, v42, 0xbc000000, v2
	v_pk_add_f32 v[6:7], v[6:7], v[8:9]
	v_mul_f32_e32 v8, v5, v5

.Lw3b105:
	v_mul_f32_e32 v14, v27, v27
	v_mul_f32_e32 v42, v2, v2
	v_mul_f32_e32 v43, v3, v3
	v_pk_fma_f32 v[8:9], v[4:5], v[4:5], v[8:9] op_sel_hi:[1,1,0]
	v_pk_fma_f32 v[14:15], v[26:27], v[26:27], v[14:15] op_sel_hi:[1,1,0]
	v_mov_b32_e32 v9, v42
	v_mov_b32_e32 v15, v43
	v_pk_add_f32 v[8:9], v[8:9], v[14:15]
	s_nop 0
	v_pk_add_f32 v[6:7], v[6:7], v[8:9]
	s_nop 0

.Lw3b106:
	v_add_f32_e32 v6, v6, v7
	ds_bpermute_b32 v7, v40, v6
	s_waitcnt lgkmcnt(0)
	v_add_f32_e32 v6, v6, v7
	ds_bpermute_b32 v7, v41, v6
	s_waitcnt lgkmcnt(0)
	v_add_f32_e32 v6, v6, v7
	v_fmamk_f32 v6, v6, 0x3c000000, v98
	v_mul_f32_e32 v7, 0x4b800000, v6
	v_cmp_gt_f32_e32 vcc, s28, v6
	s_nop 1

.Lw3b107:
	v_cndmask_b32_e32 v6, v6, v7, vcc
	v_rsq_f32_e32 v14, v6
	ds_read_b128 v[6:9], v96 offset:512
	ds_read_b128 v[40:43], v96 offset:528
	ds_read_b128 v[44:47], v96 offset:1024
	ds_read_b128 v[48:51], v96 offset:1040
	v_mul_f32_e32 v15, 0x45800000, v14
	v_cndmask_b32_e32 v30, v14, v15, vcc
	v_pk_mul_f32 v[14:15], v[30:31], v[28:29] op_sel_hi:[0,1]

.Lw3b108:
	s_waitcnt lgkmcnt(1)
	v_pk_fma_f32 v[6:7], v[6:7], v[14:15], v[44:45]
	v_pk_mul_f32 v[28:29], v[30:31], v[38:39] op_sel_hi:[0,1]
	v_pk_mul_f32 v[14:15], v[6:7], v[6:7]
	v_pk_fma_f32 v[8:9], v[8:9], v[28:29], v[46:47]
	v_fmamk_f32 v14, v14, 0xbdd2d3e8, v99
	v_fmamk_f32 v15, v15, 0xbdd2d3e8, v99
	v_mul_f32_e32 v14, v6, v14
	v_mul_f32_e32 v15, v7, v15

.Lw3b109:
	v_exp_f32_e32 v14, v14
	v_exp_f32_e32 v15, v15
	v_pk_mul_f32 v[28:29], v[8:9], v[8:9]
	v_add_f32_e32 v14, 1.0, v14
	v_add_f32_e32 v15, 1.0, v15
	v_rcp_f32_e32 v14, v14
	v_rcp_f32_e32 v15, v15
	v_fmamk_f32 v28, v28, 0xbdd2d3e8, v99
	v_mul_f32_e32 v28, v8, v28
	v_exp_f32_e32 v28, v28
	v_pk_mul_f32 v[6:7], v[6:7], v[14:15]
	v_fmamk_f32 v14, v29, 0xbdd2d3e8, v99

.Lw3b110:
	v_mul_f32_e32 v14, v9, v14
	v_exp_f32_e32 v29, v14
	v_pk_mul_f32 v[14:15], v[30:31], v[24:25] op_sel_hi:[0,1]
	s_waitcnt lgkmcnt(0)
	v_pk_fma_f32 v[14:15], v[40:41], v[14:15], v[48:49]
	v_cvt_pk_f16_f32 v6, v6, v7
	v_pk_mul_f32 v[24:25], v[14:15], v[14:15]
	v_add_f32_e32 v7, 1.0, v28
	v_fmamk_f32 v24, v24, 0xbdd2d3e8, v99

.Lw3b111:
	v_mul_f32_e32 v24, v14, v24
	v_exp_f32_e32 v24, v24
	v_rcp_f32_e32 v28, v7
	v_add_f32_e32 v7, 1.0, v29
	v_rcp_f32_e32 v29, v7
	v_add_f32_e32 v7, 1.0, v24
	v_fmamk_f32 v24, v25, 0xbdd2d3e8, v99
	v_mul_f32_e32 v31, v15, v24
	v_pk_mul_f32 v[24:25], v[30:31], v[36:37] op_sel_hi:[0,1]
	v_pk_fma_f32 v[24:25], v[42:43], v[24:25], v[50:51]
	v_exp_f32_e32 v31, v31
	v_pk_mul_f32 v[36:37], v[24:25], v[24:25]

.Lw3b112:
	v_rcp_f32_e32 v38, v7
	v_fmamk_f32 v36, v36, 0xbdd2d3e8, v99
	v_fmamk_f32 v37, v37, 0xbdd2d3e8, v99
	v_mul_f32_e32 v36, v24, v36
	v_mul_f32_e32 v37, v25, v37
	v_exp_f32_e32 v36, v36
	v_exp_f32_e32 v37, v37
	v_add_f32_e32 v7, 1.0, v31
	v_mov_b32_e32 v31, v84
	v_add_f32_e32 v36, 1.0, v36
	v_add_f32_e32 v37, 1.0, v37
	v_rcp_f32_e32 v36, v36

.Lw3b113:
	v_rcp_f32_e32 v37, v37
	v_rcp_f32_e32 v39, v7
	v_pk_mul_f32 v[8:9], v[8:9], v[28:29]
	v_pk_mul_f32 v[24:25], v[24:25], v[36:37]
	s_nop 0
	s_nop 0
	v_lshl_add_u32 v7, v31, 2, v101
	v_add_u32_e32 v52, 0x420, v7
	v_add_u32_e32 v46, 0x428, v7
	v_add_u32_e32 v50, 0x430, v7

.Lw3b114:
	ds_read2_b32 v[36:37], v7 offset0:138 offset1:139
	ds_read2_b32 v[40:41], v7 offset0:142 offset1:143
	ds_read2_b32 v[42:43], v7 offset0:140 offset1:141
	ds_read2_b32 v[44:45], v7 offset0:136 offset1:137
	v_add_u32_e32 v7, 0x438, v7
	ds_read2_b32 v[46:47], v46 offset1:1
	ds_read2_b32 v[48:49], v7 offset1:1

.Lw3b115:
	ds_read2_b32 v[50:51], v50 offset1:1
	ds_read2_b32 v[52:53], v52 offset1:1
	v_cvt_pk_f16_f32 v7, v8, v9
	v_pk_mul_f32 v[8:9], v[14:15], v[38:39]
	s_nop 0
	v_cvt_pk_f16_f32 v8, v8, v9
	v_pk_mul_f32 v[14:15], v[30:31], v[34:35] op_sel_hi:[0,1]
	s_waitcnt lgkmcnt(0)
	v_pk_fma_f32 v[14:15], v[44:45], v[14:15], v[52:53]

.Lw3b116:
	v_pk_mul_f32 v[22:23], v[30:31], v[22:23] op_sel_hi:[0,1]
	v_pk_mul_f32 v[28:29], v[14:15], v[14:15]
	v_pk_fma_f32 v[22:23], v[36:37], v[22:23], v[46:47]
	v_fmamk_f32 v9, v28, 0xbdd2d3e8, v99
	v_mul_f32_e32 v9, v14, v9
	v_fmamk_f32 v28, v29, 0xbdd2d3e8, v99
	v_exp_f32_e32 v9, v9
	v_mul_f32_e32 v28, v15, v28
	v_exp_f32_e32 v29, v28

.Lw3b117:
	v_pk_mul_f32 v[34:35], v[22:23], v[22:23]
	v_add_f32_e32 v9, 1.0, v9
	v_rcp_f32_e32 v28, v9
	v_add_f32_e32 v9, 1.0, v29
	v_rcp_f32_e32 v29, v9
	v_fmamk_f32 v9, v34, 0xbdd2d3e8, v99
	v_mul_f32_e32 v9, v22, v9
	v_exp_f32_e32 v34, v9
	v_cvt_pk_f16_f32 v9, v24, v25
	v_fmamk_f32 v24, v35, 0xbdd2d3e8, v99
	v_pk_mul_f32 v[16:17], v[30:31], v[16:17] op_sel_hi:[0,1]

.Lw3b118:
	v_mul_f32_e32 v24, v23, v24
	v_pk_fma_f32 v[16:17], v[42:43], v[16:17], v[50:51]
	v_pk_mul_f32 v[14:15], v[14:15], v[28:29]
	v_exp_f32_e32 v29, v24
	v_pk_mul_f32 v[24:25], v[16:17], v[16:17]
	v_cvt_pk_f16_f32 v14, v14, v15
	v_fmamk_f32 v24, v24, 0xbdd2d3e8, v99
	v_mul_f32_e32 v24, v16, v24
	v_exp_f32_e32 v24, v24

.Lw3b119:
	v_add_f32_e32 v15, 1.0, v34
	v_rcp_f32_e32 v28, v15
	v_add_f32_e32 v15, 1.0, v29
	v_rcp_f32_e32 v29, v15
	v_add_f32_e32 v15, 1.0, v24
	v_fmamk_f32 v24, v25, 0xbdd2d3e8, v99
	v_mul_f32_e32 v34, v17, v24
	v_pk_mul_f32 v[24:25], v[30:31], v[32:33] op_sel_hi:[0,1]
	v_pk_fma_f32 v[24:25], v[40:41], v[24:25], v[48:49]
	v_exp_f32_e32 v35, v34
	v_pk_mul_f32 v[32:33], v[24:25], v[24:25]

.Lw3b120:
	v_rcp_f32_e32 v34, v15
	v_fmamk_f32 v32, v32, 0xbdd2d3e8, v99
	v_fmamk_f32 v33, v33, 0xbdd2d3e8, v99
	v_mul_f32_e32 v32, v24, v32
	v_mul_f32_e32 v33, v25, v33
	v_exp_f32_e32 v32, v32
	v_exp_f32_e32 v33, v33
	v_add_f32_e32 v15, 1.0, v35
	v_rcp_f32_e32 v35, v15
	v_add_f32_e32 v32, 1.0, v32
	v_add_f32_e32 v33, 1.0, v33
	v_rcp_f32_e32 v32, v32
	v_rcp_f32_e32 v33, v33

.Lw3b121:
	v_pk_mul_f32 v[22:23], v[22:23], v[28:29]
	v_pk_mul_f32 v[16:17], v[16:17], v[34:35]
	v_pk_mul_f32 v[24:25], v[24:25], v[32:33]
	s_nop 0
	v_cvt_pk_f16_f32 v16, v16, v17
	v_lshl_add_u32 v15, v31, 2, v101
	v_add_u32_e32 v48, 0x440, v15
	v_add_u32_e32 v42, 0x448, v15

.Lw3b122:
	v_add_u32_e32 v46, 0x450, v15
	ds_read2_b32 v[32:33], v15 offset0:146 offset1:147
	ds_read2_b32 v[36:37], v15 offset0:150 offset1:151
	ds_read2_b32 v[38:39], v15 offset0:148 offset1:149
	ds_read2_b32 v[40:41], v15 offset0:144 offset1:145
	v_add_u32_e32 v15, 0x458, v15
	ds_read2_b32 v[42:43], v42 offset1:1
	ds_read2_b32 v[44:45], v15 offset1:1

.Lw3b123:
	ds_read2_b32 v[46:47], v46 offset1:1
	ds_read2_b32 v[48:49], v48 offset1:1
	v_cvt_pk_f16_f32 v15, v22, v23
	v_pk_mul_f32 v[12:13], v[30:31], v[12:13] op_sel_hi:[0,1]
	s_waitcnt lgkmcnt(0)
	v_pk_fma_f32 v[12:13], v[40:41], v[12:13], v[48:49]
	v_pk_mul_f32 v[18:19], v[30:31], v[18:19] op_sel_hi:[0,1]
	v_pk_mul_f32 v[22:23], v[12:13], v[12:13]

.Lw3b124:
	v_pk_fma_f32 v[28:29], v[32:33], v[18:19], v[42:43]
	v_fmamk_f32 v17, v22, 0xbdd2d3e8, v99
	v_mul_f32_e32 v17, v12, v17
	v_fmamk_f32 v22, v23, 0xbdd2d3e8, v99
	v_exp_f32_e32 v17, v17
	v_mul_f32_e32 v22, v13, v22
	v_exp_f32_e32 v23, v22
	v_pk_mul_f32 v[18:19], v[28:29], v[28:29]
	v_add_f32_e32 v17, 1.0, v17
	v_rcp_f32_e32 v22, v17

.Lw3b125:
	v_add_f32_e32 v17, 1.0, v23
	v_rcp_f32_e32 v23, v17
	v_fmamk_f32 v17, v18, 0xbdd2d3e8, v99
	v_pk_mul_f32 v[10:11], v[30:31], v[10:11] op_sel_hi:[0,1]
	v_mul_f32_e32 v17, v28, v17
	v_pk_mul_f32 v[12:13], v[12:13], v[22:23]
	v_pk_fma_f32 v[10:11], v[36:37], v[10:11], v[44:45]
	v_cvt_pk_f16_f32 v18, v12, v13
	v_fmamk_f32 v12, v19, 0xbdd2d3e8, v99

.Lw3b126:
	v_mul_f32_e32 v12, v29, v12
	v_exp_f32_e32 v19, v12
	v_pk_mul_f32 v[12:13], v[30:31], v[20:21] op_sel_hi:[0,1]
	v_pk_fma_f32 v[12:13], v[38:39], v[12:13], v[46:47]
	v_exp_f32_e32 v32, v17
	v_pk_mul_f32 v[20:21], v[12:13], v[12:13]
	v_add_f32_e32 v19, 1.0, v19
	v_fmamk_f32 v20, v20, 0xbdd2d3e8, v99
	v_mul_f32_e32 v20, v12, v20
	v_exp_f32_e32 v20, v20
	v_rcp_f32_e32 v23, v19

.Lw3b127:
	v_cvt_pk_f16_f32 v17, v24, v25
	v_add_f32_e32 v22, 1.0, v32
	v_add_f32_e32 v19, 1.0, v20
	v_fmamk_f32 v20, v21, 0xbdd2d3e8, v99
	v_mul_f32_e32 v24, v13, v20
	v_pk_mul_f32 v[20:21], v[10:11], v[10:11]
	v_exp_f32_e32 v25, v24
	v_fmamk_f32 v20, v20, 0xbdd2d3e8, v99
	v_fmamk_f32 v21, v21, 0xbdd2d3e8, v99
	v_mul_f32_e32 v20, v10, v20

.Lw3b128:
	v_mul_f32_e32 v21, v11, v21
	v_exp_f32_e32 v20, v20
	v_exp_f32_e32 v21, v21
	v_rcp_f32_e32 v24, v19
	v_add_f32_e32 v19, 1.0, v25
	v_add_f32_e32 v20, 1.0, v20
	v_add_f32_e32 v21, 1.0, v21
	v_rcp_f32_e32 v20, v20
	v_rcp_f32_e32 v21, v21
	v_rcp_f32_e32 v25, v19
	v_rcp_f32_e32 v22, v22
	v_pk_mul_f32 v[10:11], v[10:11], v[20:21]
	s_nop 0
	v_pk_mul_f32 v[12:13], v[12:13], v[24:25]

.Lw3b129:
	v_lshl_add_u32 v19, v31, 2, v101
	v_add_u32_e32 v21, 0x468, v19
	ds_read2_b32 v[32:33], v19 offset0:154 offset1:155
	ds_read2_b32 v[34:35], v19 offset0:158 offset1:159
	ds_read2_b32 v[36:37], v19 offset0:156 offset1:157
	ds_read2_b32 v[38:39], v19 offset0:152 offset1:153
	v_add_u32_e32 v20, 0x460, v19

.Lw3b130:
	v_add_u32_e32 v31, 0x470, v19
	v_add_u32_e32 v19, 0x478, v19
	ds_read2_b32 v[40:41], v21 offset1:1
	ds_read2_b32 v[42:43], v19 offset1:1
	ds_read2_b32 v[44:45], v31 offset1:1
	ds_read2_b32 v[46:47], v20 offset1:1
	v_pk_mul_f32 v[20:21], v[28:29], v[22:23]
	s_nop 0

.Lw3b131:
	v_cvt_pk_f16_f32 v19, v20, v21
	v_cvt_pk_f16_f32 v20, v12, v13
	v_pk_mul_f32 v[4:5], v[30:31], v[4:5] op_sel_hi:[0,1]
	s_waitcnt lgkmcnt(0)
	v_pk_fma_f32 v[4:5], v[38:39], v[4:5], v[46:47]
	v_cvt_pk_f16_f32 v21, v10, v11
	v_pk_mul_f32 v[12:13], v[4:5], v[4:5]
	v_pk_mul_f32 v[10:11], v[30:31], v[26:27] op_sel_hi:[0,1]

.Lw3b132:
	v_fmamk_f32 v12, v12, 0xbdd2d3e8, v99
	v_fmamk_f32 v13, v13, 0xbdd2d3e8, v99
	v_mul_f32_e32 v12, v4, v12
	v_mul_f32_e32 v13, v5, v13
	v_exp_f32_e32 v12, v12
	v_exp_f32_e32 v13, v13
	v_pk_fma_f32 v[10:11], v[32:33], v[10:11], v[40:41]
	v_pk_mul_f32 v[0:1], v[30:31], v[0:1] op_sel_hi:[0,1]
	v_add_f32_e32 v12, 1.0, v12
	v_add_f32_e32 v13, 1.0, v13
	v_rcp_f32_e32 v12, v12

.Lw3b133:
	v_rcp_f32_e32 v13, v13
	v_pk_fma_f32 v[0:1], v[36:37], v[0:1], v[44:45]
	v_pk_mul_f32 v[2:3], v[30:31], v[2:3] op_sel_hi:[0,1]
	v_pk_fma_f32 v[2:3], v[34:35], v[2:3], v[42:43]
	v_pk_mul_f32 v[4:5], v[4:5], v[12:13]
	v_pk_mul_f32 v[12:13], v[10:11], v[10:11]
	v_cvt_pk_f16_f32 v24, v4, v5
	v_fmamk_f32 v12, v12, 0xbdd2d3e8, v99

.Lw3b134:
	v_fmamk_f32 v13, v13, 0xbdd2d3e8, v99
	v_mul_f32_e32 v12, v10, v12
	v_mul_f32_e32 v13, v11, v13
	v_exp_f32_e32 v12, v12
	v_exp_f32_e32 v13, v13
	v_add_f32_e32 v4, 1.0, v12
	v_add_f32_e32 v5, 1.0, v13
	v_pk_mul_f32 v[12:13], v[0:1], v[0:1]
	v_rcp_f32_e32 v4, v4
	v_fmamk_f32 v12, v12, 0xbdd2d3e8, v99
	v_fmamk_f32 v13, v13, 0xbdd2d3e8, v99

.Lw3b135:
	v_mul_f32_e32 v12, v0, v12
	v_mul_f32_e32 v13, v1, v13
	v_rcp_f32_e32 v5, v5
	v_exp_f32_e32 v12, v12
	v_exp_f32_e32 v13, v13
	v_pk_mul_f32 v[4:5], v[10:11], v[4:5]
	v_add_f32_e32 v10, 1.0, v12
	v_add_f32_e32 v11, 1.0, v13
	v_pk_mul_f32 v[12:13], v[2:3], v[2:3]
	v_rcp_f32_e32 v10, v10
	v_fmamk_f32 v12, v12, 0xbdd2d3e8, v99
	v_fmamk_f32 v13, v13, 0xbdd2d3e8, v99

.Lw3b136:
	v_mul_f32_e32 v12, v2, v12
	v_mul_f32_e32 v13, v3, v13
	v_exp_f32_e32 v12, v12
	v_exp_f32_e32 v13, v13
	v_rcp_f32_e32 v11, v11
	v_cvt_pk_f16_f32 v25, v4, v5
	v_add_f32_e32 v12, 1.0, v12
	v_add_f32_e32 v13, 1.0, v13
	v_rcp_f32_e32 v12, v12
	v_rcp_f32_e32 v13, v13
	v_pk_mul_f32 v[0:1], v[0:1], v[10:11]
	s_nop 0

.Lw3b137:
	v_cvt_pk_f16_f32 v26, v0, v1
	v_pk_mul_f32 v[0:1], v[2:3], v[12:13]
	s_nop 0
	v_cvt_pk_f16_f32 v27, v0, v1
	ds_read_b128 v[0:3], v96 offset:1536
	ds_read_b128 v[10:13], v96 offset:1552
	ds_read_b128 v[30:33], v96 offset:1568
	ds_read_b128 v[34:37], v96 offset:1584

.Lw3b138:
	ds_read_b128 v[38:41], v96 offset:1600
	ds_read_b128 v[42:45], v96 offset:1616
	ds_read_b128 v[46:49], v96 offset:1632
	ds_read_b128 v[50:53], v96 offset:1648
	v_mov_b32_e32 v4, v77
	s_nop 0
	v_lshl_add_u32 v28, v4, 4, v102
	ds_read_b128 v[54:57], v28
	ds_read_b128 v[58:61], v28 offset:1024

.Lw3b139:
	ds_read_b128 v[62:65], v28 offset:2048
	ds_read_b128 v[66:69], v28 offset:3072
	ds_read_b128 v[104:107], v28 offset:4096
	ds_read_b128 v[108:111], v28 offset:5120
	ds_read_b128 v[112:115], v28 offset:6144
	ds_read_b128 v[116:119], v28 offset:7168
	s_waitcnt lgkmcnt(7)
	v_mfma_f32_16x16x32_f16 v[0:3], v[54:57], v[6:9], v[0:3]

.Lw3b140:
	s_waitcnt lgkmcnt(6)
	v_mfma_f32_16x16x32_f16 v[10:13], v[58:61], v[6:9], v[10:13]
	s_waitcnt lgkmcnt(5)
	v_mfma_f32_16x16x32_f16 v[30:33], v[62:65], v[6:9], v[30:33]
	s_waitcnt lgkmcnt(4)
	v_mfma_f32_16x16x32_f16 v[34:37], v[66:69], v[6:9], v[34:37]
	ds_read_b128 v[54:57], v28 offset:8192
	ds_read_b128 v[58:61], v28 offset:9216
	ds_read_b128 v[62:65], v28 offset:10240

.Lw3b141:
	ds_read_b128 v[66:69], v28 offset:11264
	s_waitcnt lgkmcnt(7)
	v_mfma_f32_16x16x32_f16 v[38:41], v[104:107], v[6:9], v[38:41]
	s_waitcnt lgkmcnt(6)
	v_mfma_f32_16x16x32_f16 v[42:45], v[108:111], v[6:9], v[42:45]
	s_waitcnt lgkmcnt(5)
	v_mfma_f32_16x16x32_f16 v[46:49], v[112:115], v[6:9], v[46:49]
	s_waitcnt lgkmcnt(4)
	v_mfma_f32_16x16x32_f16 v[4:7], v[116:119], v[6:9], v[50:53]

.Lw3b142:
	s_nop 2
	ds_read_b128 v[50:53], v28 offset:12288
	ds_read_b128 v[104:107], v28 offset:13312
	ds_read_b128 v[108:111], v28 offset:14336
	ds_read_b128 v[112:115], v28 offset:15360
	s_waitcnt lgkmcnt(7)
	v_mfma_f32_16x16x32_f16 v[0:3], v[54:57], v[14:17], v[0:3]
	s_waitcnt lgkmcnt(6)
	v_mfma_f32_16x16x32_f16 v[8:11], v[58:61], v[14:17], v[10:13]

.Lw3b143:
	s_waitcnt lgkmcnt(5)
	v_mfma_f32_16x16x32_f16 v[30:33], v[62:65], v[14:17], v[30:33]
	s_waitcnt lgkmcnt(4)
	v_mfma_f32_16x16x32_f16 v[34:37], v[66:69], v[14:17], v[34:37]
	ds_read_b128 v[54:57], v28 offset:16384
	ds_read_b128 v[58:61], v28 offset:17408
	ds_read_b128 v[62:65], v28 offset:18432
	ds_read_b128 v[66:69], v28 offset:19456
	s_waitcnt lgkmcnt(7)

.Lw3b144:
	v_mfma_f32_16x16x32_f16 v[38:41], v[50:53], v[14:17], v[38:41]
	s_waitcnt lgkmcnt(6)
	v_mfma_f32_16x16x32_f16 v[42:45], v[104:107], v[14:17], v[42:45]
	s_waitcnt lgkmcnt(5)
	v_mfma_f32_16x16x32_f16 v[46:49], v[108:111], v[14:17], v[46:49]
	s_waitcnt lgkmcnt(4)
	v_mfma_f32_16x16x32_f16 v[4:7], v[112:115], v[14:17], v[4:7]
	ds_read_b128 v[12:15], v28 offset:20480
	ds_read_b128 v[50:53], v28 offset:21504

.Lw3b145:
	ds_read_b128 v[104:107], v28 offset:22528
	ds_read_b128 v[108:111], v28 offset:23552
	s_waitcnt lgkmcnt(7)
	v_mfma_f32_16x16x32_f16 v[0:3], v[54:57], v[18:21], v[0:3]
	s_waitcnt lgkmcnt(6)
	v_mfma_f32_16x16x32_f16 v[8:11], v[58:61], v[18:21], v[8:11]
	s_waitcnt lgkmcnt(5)
	v_mfma_f32_16x16x32_f16 v[30:33], v[62:65], v[18:21], v[30:33]
	s_waitcnt lgkmcnt(4)
	v_mfma_f32_16x16x32_f16 v[34:37], v[66:69], v[18:21], v[34:37]

.Lw3b146:
	ds_read_b128 v[54:57], v28 offset:24576
	ds_read_b128 v[58:61], v28 offset:25600
	ds_read_b128 v[62:65], v28 offset:26624
	ds_read_b128 v[66:69], v28 offset:27648
	s_waitcnt lgkmcnt(7)
	v_mfma_f32_16x16x32_f16 v[12:15], v[12:15], v[18:21], v[38:41]
	s_waitcnt lgkmcnt(6)
	v_mfma_f32_16x16x32_f16 v[38:41], v[50:53], v[18:21], v[42:45]

.Lw3b147:
	s_waitcnt lgkmcnt(5)
	v_mfma_f32_16x16x32_f16 v[42:45], v[104:107], v[18:21], v[46:49]
	s_waitcnt lgkmcnt(4)
	v_mfma_f32_16x16x32_f16 v[46:49], v[108:111], v[18:21], v[4:7]
	s_nop 2
	ds_read_b128 v[4:7], v28 offset:28672
	ds_read_b128 v[50:53], v28 offset:29696
	ds_read_b128 v[104:107], v28 offset:30720
	ds_read_b128 v[108:111], v28 offset:31744

.Lw3b148:
	s_waitcnt lgkmcnt(7)
	v_mfma_f32_16x16x32_f16 v[54:57], v[54:57], v[24:27], v[0:3]
	s_waitcnt lgkmcnt(6)
	v_mfma_f32_16x16x32_f16 v[58:61], v[58:61], v[24:27], v[8:11]
	s_waitcnt lgkmcnt(5)
	v_mfma_f32_16x16x32_f16 v[20:23], v[62:65], v[24:27], v[30:33]
	s_waitcnt lgkmcnt(4)
	v_mfma_f32_16x16x32_f16 v[16:19], v[66:69], v[24:27], v[34:37]
	s_waitcnt lgkmcnt(0)
	v_mfma_f32_16x16x32_f16 v[0:3], v[108:111], v[24:27], v[46:49]

.Lw3b149:
	v_mfma_f32_16x16x32_f16 v[12:15], v[4:7], v[24:27], v[12:15]
	v_mfma_f32_16x16x32_f16 v[8:11], v[50:53], v[24:27], v[38:41]
	v_mfma_f32_16x16x32_f16 v[4:7], v[104:107], v[24:27], v[42:45]
	v_mul_f32_e32 v24, v54, v54
	v_fmamk_f32 v24, v24, 0xbdd2d3e8, v99
	v_mul_f32_e32 v24, v54, v24
	v_exp_f32_e32 v24, v24
	v_mul_f32_e32 v25, v55, v55
	v_mul_f32_e32 v26, v56, v56
	v_fmamk_f32 v25, v25, 0xbdd2d3e8, v99

.Lw3b150:
	v_fmamk_f32 v26, v26, 0xbdd2d3e8, v99
	v_mul_f32_e32 v25, v55, v25
	v_add_f32_e32 v24, 1.0, v24
	v_mul_f32_e32 v26, v56, v26
	v_rcp_f32_e32 v24, v24
	v_exp_f32_e32 v25, v25
	v_exp_f32_e32 v26, v26
	v_mul_f32_e32 v30, v57, v57
	v_mul_f32_e32 v31, v58, v58
	v_fmamk_f32 v30, v30, 0xbdd2d3e8, v99
	v_fmamk_f32 v31, v31, 0xbdd2d3e8, v99
	v_fma_mixlo_f16 v29, v54, v24, 0

.Lw3b151:
	v_add_f32_e32 v24, 1.0, v25
	v_add_f32_e32 v25, 1.0, v26
	v_mul_f32_e32 v30, v57, v30
	v_mul_f32_e32 v31, v58, v31
	v_rcp_f32_e32 v24, v24
	v_rcp_f32_e32 v25, v25
	v_exp_f32_e32 v30, v30
	v_exp_f32_e32 v31, v31
	v_mov_b32_e32 v26, v55
	v_mov_b32_e32 v27, v56
	v_pk_mul_f32 v[24:25], v[26:27], v[24:25]
	v_add_f32_e32 v26, 1.0, v30
	v_add_f32_e32 v27, 1.0, v31

.Lw3b152:
	v_rcp_f32_e32 v26, v26
	v_rcp_f32_e32 v27, v27
	v_cvt_pk_f16_f32 v25, v24, v25
	v_pk_mov_b32 v[30:31], v[56:57], v[58:59] op_sel:[1,0]
	v_pack_b32_f16 v24, v29, v25
	v_pk_mul_f32 v[26:27], v[30:31], v[26:27]
	v_mul_f32_e32 v29, v59, v59
	v_mul_f32_e32 v30, v60, v60
	v_fmamk_f32 v29, v29, 0xbdd2d3e8, v99
	v_fmamk_f32 v30, v30, 0xbdd2d3e8, v99

.Lw3b153:
	v_mul_f32_e32 v29, v59, v29
	v_mul_f32_e32 v30, v60, v30
	v_exp_f32_e32 v29, v29
	v_exp_f32_e32 v30, v30
	v_cvt_pk_f16_f32 v32, v26, v27
	v_mov_b32_e32 v31, v60
	v_add_f32_e32 v26, 1.0, v29
	v_add_f32_e32 v27, 1.0, v30
	v_rcp_f32_e32 v26, v26
	v_rcp_f32_e32 v27, v27
	v_mov_b32_e32 v30, v59
	v_alignbit_b32 v25, v32, v25, 16

.Lw3b154:
	v_mul_f32_e32 v34, v20, v20
	v_pk_mul_f32 v[26:27], v[30:31], v[26:27]
	v_fmamk_f32 v34, v34, 0xbdd2d3e8, v99
	v_cvt_pk_f16_f32 v27, v26, v27
	v_mul_f32_e32 v26, v61, v61
	v_fmamk_f32 v26, v26, 0xbdd2d3e8, v99
	v_mul_f32_e32 v26, v61, v26
	v_exp_f32_e32 v29, v26
	v_alignbit_b32 v26, v27, v32, 16
	ds_read_b128 v[30:33], v28 offset:32768

.Lw3b155:
	v_mul_f32_e32 v34, v20, v34
	v_add_f32_e32 v29, 1.0, v29
	v_rcp_f32_e32 v29, v29
	v_lshrrev_b32_e32 v27, 16, v27
	v_exp_f32_e32 v38, v34
	ds_read_b128 v[34:37], v28 offset:33792
	v_fma_mixhi_f16 v27, v61, v29, 0
	v_add_f32_e32 v29, 1.0, v38
	s_waitcnt lgkmcnt(1)
	v_mfma_f32_16x16x32_f16 v[24:27], v[30:33], v[24:27], 0
	v_mul_f32_e32 v30, v21, v21

.Lw3b156:
	v_fmamk_f32 v30, v30, 0xbdd2d3e8, v99
	v_mul_f32_e32 v31, v22, v22
	v_mul_f32_e32 v30, v21, v30
	v_fmamk_f32 v31, v31, 0xbdd2d3e8, v99
	v_rcp_f32_e32 v29, v29
	v_exp_f32_e32 v30, v30
	v_mul_f32_e32 v31, v22, v31
	v_exp_f32_e32 v31, v31
	v_fma_mixlo_f16 v29, v20, v29, 0
	v_add_f32_e32 v20, 1.0, v30
	v_rcp_f32_e32 v30, v20
	v_add_f32_e32 v20, 1.0, v31

.Lw3b157:
	v_rcp_f32_e32 v31, v20
	v_mov_b32_e32 v20, v21
	v_mov_b32_e32 v21, v22
	v_mul_f32_e32 v22, v23, v23
	v_fmamk_f32 v22, v22, 0xbdd2d3e8, v99
	v_mul_f32_e32 v32, v16, v16
	v_mul_f32_e32 v22, v23, v22
	v_fmamk_f32 v32, v32, 0xbdd2d3e8, v99
	v_exp_f32_e32 v22, v22
	v_mul_f32_e32 v32, v16, v32
	v_exp_f32_e32 v32, v32
	v_pk_mul_f32 v[20:21], v[20:21], v[30:31]

.Lw3b158:
	v_add_f32_e32 v22, 1.0, v22
	v_rcp_f32_e32 v30, v22
	v_add_f32_e32 v22, 1.0, v32
	v_rcp_f32_e32 v31, v22
	v_pk_mov_b32 v[22:23], v[22:23], v[16:17] op_sel:[1,0]
	v_cvt_pk_f16_f32 v21, v20, v21
	v_mul_f32_e32 v16, v17, v17
	v_pk_mul_f32 v[22:23], v[22:23], v[30:31]
	v_pack_b32_f16 v20, v29, v21
	v_cvt_pk_f16_f32 v29, v22, v23

.Lw3b159:
	v_fmamk_f32 v16, v16, 0xbdd2d3e8, v99
	v_mul_f32_e32 v22, v18, v18
	v_mul_f32_e32 v16, v17, v16
	v_fmamk_f32 v22, v22, 0xbdd2d3e8, v99
	v_exp_f32_e32 v16, v16
	v_mul_f32_e32 v22, v18, v22
	v_exp_f32_e32 v23, v22
	v_alignbit_b32 v21, v29, v21, 16
	v_add_f32_e32 v16, 1.0, v16
	v_rcp_f32_e32 v22, v16
	v_add_f32_e32 v16, 1.0, v23
	v_rcp_f32_e32 v23, v16

.Lw3b160:
	v_mul_f32_e32 v16, v19, v19
	v_fmamk_f32 v16, v16, 0xbdd2d3e8, v99
	v_mul_f32_e32 v16, v19, v16
	v_exp_f32_e32 v30, v16
	v_mov_b32_e32 v16, v17
	v_mov_b32_e32 v17, v18
	v_pk_mul_f32 v[16:17], v[16:17], v[22:23]
	v_add_f32_e32 v18, 1.0, v30
	v_rcp_f32_e32 v18, v18
	v_cvt_pk_f16_f32 v16, v16, v17
	v_lshrrev_b32_e32 v23, 16, v16
	v_alignbit_b32 v22, v16, v29, 16

.Lw3b161:
	v_fma_mixhi_f16 v23, v19, v18, 0
	s_waitcnt lgkmcnt(0)
	s_nop 0
	v_mfma_f32_16x16x32_f16 v[16:19], v[34:37], v[20:23], v[24:27]
	v_mul_f32_e32 v20, v12, v12
	v_fmamk_f32 v20, v20, 0xbdd2d3e8, v99
	v_mul_f32_e32 v20, v12, v20
	v_exp_f32_e32 v20, v20
	v_mul_f32_e32 v21, v13, v13
	v_fmamk_f32 v21, v21, 0xbdd2d3e8, v99

.Lw3b162:
	v_mul_f32_e32 v22, v14, v14
	v_mul_f32_e32 v21, v13, v21
	v_add_f32_e32 v20, 1.0, v20
	v_fmamk_f32 v22, v22, 0xbdd2d3e8, v99
	v_rcp_f32_e32 v20, v20
	v_exp_f32_e32 v21, v21
	v_mul_f32_e32 v22, v14, v22
	v_exp_f32_e32 v22, v22
	v_fma_mixlo_f16 v23, v12, v20, 0
	v_add_f32_e32 v12, 1.0, v21
	v_rcp_f32_e32 v20, v12
	v_add_f32_e32 v12, 1.0, v22
	v_rcp_f32_e32 v21, v12

.Lw3b163:
	v_mov_b32_e32 v12, v13
	v_mov_b32_e32 v13, v14
	v_mul_f32_e32 v14, v15, v15
	v_fmamk_f32 v14, v14, 0xbdd2d3e8, v99
	v_mul_f32_e32 v22, v8, v8
	v_mul_f32_e32 v14, v15, v14
	v_fmamk_f32 v22, v22, 0xbdd2d3e8, v99
	v_exp_f32_e32 v14, v14
	v_mul_f32_e32 v22, v8, v22
	v_exp_f32_e32 v22, v22
	v_pk_mul_f32 v[12:13], v[12:13], v[20:21]
	v_add_f32_e32 v14, 1.0, v14

.Lw3b164:
	v_rcp_f32_e32 v20, v14
	v_add_f32_e32 v14, 1.0, v22
	v_rcp_f32_e32 v21, v14
	v_pk_mov_b32 v[14:15], v[14:15], v[8:9] op_sel:[1,0]
	v_mul_f32_e32 v8, v9, v9
	v_fmamk_f32 v8, v8, 0xbdd2d3e8, v99
	v_pk_mul_f32 v[14:15], v[14:15], v[20:21]
	v_mul_f32_e32 v20, v10, v10
	v_mul_f32_e32 v8, v9, v8
	v_fmamk_f32 v20, v20, 0xbdd2d3e8, v99
	v_exp_f32_e32 v8, v8

.Lw3b165:
	v_mul_f32_e32 v20, v10, v20
	v_exp_f32_e32 v20, v20
	v_cvt_pk_f16_f32 v21, v14, v15
	v_add_f32_e32 v8, 1.0, v8
	v_rcp_f32_e32 v14, v8
	v_add_f32_e32 v8, 1.0, v20
	v_rcp_f32_e32 v15, v8
	v_mov_b32_e32 v8, v9
	v_mov_b32_e32 v9, v10
	v_cvt_pk_f16_f32 v13, v12, v13
	v_pk_mul_f32 v[8:9], v[8:9], v[14:15]
	v_pack_b32_f16 v12, v23, v13

.Lw3b166:
	v_cvt_pk_f16_f32 v8, v8, v9
	v_mul_f32_e32 v9, v11, v11
	v_fmamk_f32 v9, v9, 0xbdd2d3e8, v99
	v_mul_f32_e32 v9, v11, v9
	v_exp_f32_e32 v9, v9
	v_alignbit_b32 v13, v21, v13, 16
	v_alignbit_b32 v14, v8, v21, 16
	ds_read_b128 v[20:23], v28 offset:34816
	v_lshrrev_b32_e32 v15, 16, v8

.Lw3b167:
	v_add_f32_e32 v8, 1.0, v9
	v_rcp_f32_e32 v8, v8
	v_mul_f32_e32 v9, v4, v4
	v_fmamk_f32 v9, v9, 0xbdd2d3e8, v99
	v_mul_f32_e32 v9, v4, v9
	v_exp_f32_e32 v24, v9
	v_fma_mixhi_f16 v15, v11, v8, 0
	ds_read_b128 v[8:11], v28 offset:35840
	s_waitcnt lgkmcnt(1)
	v_mfma_f32_16x16x32_f16 v[12:15], v[20:23], v[12:15], v[16:19]
	s_nop 2

.Lw3b168:
	v_mul_f32_e32 v17, v5, v5
	v_fmamk_f32 v17, v17, 0xbdd2d3e8, v99
	v_mul_f32_e32 v18, v6, v6
	v_add_f32_e32 v16, 1.0, v24
	v_mul_f32_e32 v17, v5, v17
	v_fmamk_f32 v18, v18, 0xbdd2d3e8, v99
	v_rcp_f32_e32 v16, v16
	v_exp_f32_e32 v17, v17
	v_mul_f32_e32 v18, v6, v18
	v_exp_f32_e32 v18, v18
	v_fma_mixlo_f16 v19, v4, v16, 0
	v_add_f32_e32 v4, 1.0, v17

.Lw3b169:
	v_rcp_f32_e32 v16, v4
	v_add_f32_e32 v4, 1.0, v18
	v_rcp_f32_e32 v17, v4
	v_mov_b32_e32 v4, v5
	v_mov_b32_e32 v5, v6
	v_mul_f32_e32 v6, v7, v7
	v_fmamk_f32 v6, v6, 0xbdd2d3e8, v99
	v_mul_f32_e32 v18, v0, v0
	v_mul_f32_e32 v6, v7, v6
	v_fmamk_f32 v18, v18, 0xbdd2d3e8, v99
	v_exp_f32_e32 v6, v6
	v_mul_f32_e32 v18, v0, v18
	v_exp_f32_e32 v18, v18

.Lw3b170:
	v_pk_mul_f32 v[4:5], v[4:5], v[16:17]
	v_add_f32_e32 v6, 1.0, v6
	v_rcp_f32_e32 v16, v6
	v_add_f32_e32 v6, 1.0, v18
	v_rcp_f32_e32 v17, v6
	v_pk_mov_b32 v[6:7], v[6:7], v[0:1] op_sel:[1,0]
	v_mul_f32_e32 v0, v1, v1
	v_fmamk_f32 v0, v0, 0xbdd2d3e8, v99
	v_pk_mul_f32 v[6:7], v[6:7], v[16:17]
	v_mul_f32_e32 v0, v1, v0
	v_cvt_pk_f16_f32 v16, v6, v7

.Lw3b171:
	v_mul_f32_e32 v6, v2, v2
	v_fmamk_f32 v6, v6, 0xbdd2d3e8, v99
	v_exp_f32_e32 v0, v0
	v_mul_f32_e32 v6, v2, v6
	v_exp_f32_e32 v7, v6
	v_cvt_pk_f16_f32 v5, v4, v5
	v_add_f32_e32 v0, 1.0, v0
	v_rcp_f32_e32 v6, v0
	v_add_f32_e32 v0, 1.0, v7
	v_rcp_f32_e32 v7, v0
	v_mul_f32_e32 v0, v3, v3
	v_fmamk_f32 v0, v0, 0xbdd2d3e8, v99

.Lw3b172:
	v_mul_f32_e32 v0, v3, v0
	v_exp_f32_e32 v17, v0
	v_mov_b32_e32 v0, v1
	v_mov_b32_e32 v1, v2
	v_pk_mul_f32 v[0:1], v[0:1], v[6:7]
	v_add_f32_e32 v2, 1.0, v17
	v_rcp_f32_e32 v2, v2
	v_cvt_pk_f16_f32 v0, v0, v1
	v_lshrrev_b32_e32 v7, 16, v0
	v_pack_b32_f16 v4, v19, v5
	v_alignbit_b32 v5, v16, v5, 16

.Lw3b173:
	v_alignbit_b32 v6, v0, v16, 16
	v_fma_mixhi_f16 v7, v3, v2, 0
	s_waitcnt lgkmcnt(0)
	s_nop 0
	v_mfma_f32_16x16x32_f16 v[0:3], v[8:11], v[4:7], v[12:15]
	s_and_saveexec_b64 s[14:15], s[4:5]
	s_xor_b64 s[14:15], exec, s[14:15]
	s_cbranch_execz .LBB3_9
	s_load_dwordx2 s[20:21], s[16:17], 0x0
	s_nop 3

.Lw3b174:
	v_or_b32_e32 v2, s10, v80
	v_ashrrev_i32_e32 v3, 31, v2
	v_lshl_add_u64 v[2:3], v[2:3], 3, s[6:7]
	s_waitcnt lgkmcnt(0)
	v_pk_add_f32 v[0:1], v[0:1], s[20:21]
	global_store_dwordx2 v[2:3], v[0:1], off
	s_branch .LBB3_9
